# speedup vs baseline: 1.0931x; 1.0931x over previous
.LBB4_110:
	s_endpgm
	s_nop 0
	s_nop 0
	s_nop 0
	s_nop 0
	s_nop 0
	s_nop 0
	s_nop 0
	s_nop 0
	s_nop 0
	s_nop 0
	s_nop 0
	s_nop 0
	s_nop 0
	s_nop 0
	s_nop 0
	s_nop 0
	s_nop 0
	s_nop 0
	s_nop 0
	s_endpgm

.LBB5_96:
	s_andn2_b64 vcc, exec, s[4:5]
	s_cbranch_vccnz .LBB5_143
	s_setprio 3
	s_load_dwordx2 s[8:9], s[0:1], 0x0
	s_load_dwordx2 s[10:11], s[0:1], 0x8
	s_load_dwordx2 s[12:13], s[0:1], 0x18
	s_load_dwordx2 s[32:33], s[0:1], 0x28
	s_load_dwordx4 s[36:39], s[0:1], 0x30
	s_load_dwordx2 s[18:19], s[0:1], 0xb8
	s_load_dwordx2 s[16:17], s[0:1], 0xc8
	s_load_dword s34, s[0:1], 0xd4
	s_lshr_b32 s3, s2, 4
	s_bfe_u32 s4, s2, 0x10003
	s_and_b32 s5, s2, 7
	v_lshrrev_b32_e32 v1, 6, v0
	v_and_b32_e32 v2, 63, v0
	v_and_b32_e32 v3, 15, v0
	v_bfe_u32 v4, v0, 4, 2
	s_nop 1
	v_readfirstlane_b32 s6, v1
	s_waitcnt lgkmcnt(0)
	s_cmp_eq_u32 s3, 0
	s_cselect_b32 s12, s12, s32
	s_cselect_b32 s13, s13, s33
	s_cselect_b32 s14, s36, s38
	s_cselect_b32 s15, s37, s39
	s_mul_i32 s35, s4, 0x708
	s_add_u32 s12, s12, s35
	s_addc_u32 s13, s13, 0
	s_mul_i32 s35, s5, 0x25800
	s_add_u32 s14, s14, s35
	s_addc_u32 s15, s15, 0
	s_mul_i32 s35, s4, 0x258
	s_add_u32 s14, s14, s35
	s_addc_u32 s15, s15, 0
	s_lshl_b64 s[10:11], s[10:11], 2
	s_mul_i32 s35, s3, 0x384000
	s_add_u32 s8, s8, s35
	s_addc_u32 s9, s9, 0
	s_mul_i32 s35, s5, 0x70800
	s_add_u32 s8, s8, s35
	s_addc_u32 s9, s9, 0
	s_mul_i32 s35, s4, 0x708
	s_add_u32 s8, s8, s35
	s_addc_u32 s9, s9, 0
	s_mul_i32 s35, s4, 112
	s_lshl_b32 s40, s6, 1
	s_add_i32 s35, s35, s40
	s_mul_i32 s35, s35, 0xe10
	s_add_u32 s22, s8, s35
	s_addc_u32 s23, s9, 0
	s_add_u32 s46, s22, 0xe10
	s_addc_u32 s47, s23, 0
	s_cmp_eq_u32 s4, 0
	s_mov_b32 s27, 0xffff1f00
	s_mov_b32 s20, 0xfffffb50
	s_cselect_b32 s27, 0xe100, s27
	s_cselect_b32 s50, 0, -1
	s_cselect_b32 s20, 0x4b0, s20
	s_cselect_b32 s21, 0, -1
	s_lshl_b32 s35, s3, 1
	s_add_i32 s35, s35, s4
	s_add_i32 s35, s35, s34
	s_mul_i32 s35, s35, 0x28000
	s_add_u32 s16, s16, s35
	s_addc_u32 s17, s17, 0
	s_mul_i32 s35, s6, 0x5000
	s_add_u32 s16, s16, s35
	s_addc_u32 s17, s17, 0
	s_mov_b32 s28, 0xffff
	s_mov_b32 s29, 0
	s_mov_b32 s30, -1
	s_mov_b32 s31, 1
	s_mov_b32 s51, 0xbfb8aa3b
	s_mov_b32 s52, 0x4038aa3b
	v_lshlrev_b32_e32 v5, 4, v2
	v_mov_b32_e32 v36, 0
	v_mov_b32_e32 v37, 0
	v_mov_b32_e32 v38, 0
	v_mov_b32_e32 v39, 0
	v_mov_b32_e32 v60, 0
	v_mov_b32_e32 v61, 0
	v_mov_b32_e32 v62, 0
	v_mov_b32_e32 v63, 0
	v_mov_b32_e32 v84, 0
	v_mov_b32_e32 v85, 0
	v_mov_b32_e32 v86, 0
	v_mov_b32_e32 v87, 0
	v_mov_b32_e32 v108, 0
	v_mov_b32_e32 v109, 0
	v_mov_b32_e32 v110, 0
	v_mov_b32_e32 v111, 0
	s_add_u32 s42, s16, 0x0
	s_addc_u32 s43, s17, 0
	global_load_dwordx4 v[16:19], v5, s[42:43] offset:0
	global_load_dwordx4 v[20:23], v5, s[42:43] offset:1024
	global_load_dwordx4 v[24:27], v5, s[42:43] offset:2048
	global_load_dwordx4 v[28:31], v5, s[42:43] offset:3072
	s_add_u32 s42, s16, 0x1000
	s_addc_u32 s43, s17, 0
	global_load_dwordx4 v[32:35], v5, s[42:43]
	s_add_u32 s42, s16, 0x1400
	s_addc_u32 s43, s17, 0
	global_load_dwordx4 v[40:43], v5, s[42:43] offset:0
	global_load_dwordx4 v[44:47], v5, s[42:43] offset:1024
	global_load_dwordx4 v[48:51], v5, s[42:43] offset:2048
	global_load_dwordx4 v[52:55], v5, s[42:43] offset:3072
	s_add_u32 s42, s16, 0x2400
	s_addc_u32 s43, s17, 0
	global_load_dwordx4 v[56:59], v5, s[42:43]
	s_add_u32 s42, s16, 0x2800
	s_addc_u32 s43, s17, 0
	global_load_dwordx4 v[64:67], v5, s[42:43] offset:0
	global_load_dwordx4 v[68:71], v5, s[42:43] offset:1024
	global_load_dwordx4 v[72:75], v5, s[42:43] offset:2048
	global_load_dwordx4 v[76:79], v5, s[42:43] offset:3072
	s_add_u32 s42, s16, 0x3800
	s_addc_u32 s43, s17, 0
	global_load_dwordx4 v[80:83], v5, s[42:43]
	s_add_u32 s42, s16, 0x3c00
	s_addc_u32 s43, s17, 0
	global_load_dwordx4 v[88:91], v5, s[42:43] offset:0
	global_load_dwordx4 v[92:95], v5, s[42:43] offset:1024
	global_load_dwordx4 v[96:99], v5, s[42:43] offset:2048
	global_load_dwordx4 v[100:103], v5, s[42:43] offset:3072
	s_add_u32 s42, s16, 0x4c00
	s_addc_u32 s43, s17, 0
	global_load_dwordx4 v[104:107], v5, s[42:43]
	v_and_b32_e32 v6, 1, v3
	v_cmp_eq_u32_e32 vcc, 1, v6
	v_mov_b32_e32 v7, 0x44444444
	v_mov_b32_e32 v8, 0xeeeeeeee
	s_nop 1
	v_cndmask_b32_e32 v112, v7, v8, vcc
	s_mul_i32 s53, s6, 19
	v_add_u32_e32 v6, s53, v3
	v_cmp_gt_u32_e32 vcc, 0x96, v6
	v_add_u32_e32 v7, 0x12c, v6
	v_mov_b32_e32 v8, 0x12c
	s_nop 1
	v_cndmask_b32_e32 v7, v8, v7, vcc
	v_lshlrev_b32_e32 v7, 2, v7
	global_load_dword v9, v7, s[12:13]
	s_mov_b64 s[54:55], vcc
	v_cmp_gt_u32_e32 vcc, 0xc0, v0
	v_lshlrev_b32_e32 v10, 2, v0
	v_mov_b32_e32 v11, 0
	s_and_saveexec_b64 s[44:45], vcc
	ds_write_b32 v10, v11 offset:61440
	s_mov_b64 exec, s[44:45]
	v_and_b32_e32 v10, 31, v0
	v_lshrrev_b32_e32 v11, 5, v0
	v_subrev_u32_e32 v12, 6, v10
	v_max_i32_e32 v12, 0, v12
	v_mul_u32_u24_e32 v13, 11, v12
	v_lshrrev_b32_e32 v13, 5, v13
	v_mul_u32_u24_e32 v14, 3, v13
	v_sub_u32_e32 v14, v12, v14
	v_mul_u32_u24_e32 v15, 19, v13
	v_add3_u32 v15, v15, v14, 16
	v_cmp_gt_u32_e32 vcc, 0x96, v15
	v_cmp_lt_u32_e64 s[56:57], 5, v10
	v_cmp_gt_u32_e64 s[58:59], 30, v10
	s_and_b64 s[56:57], s[56:57], vcc
	s_and_b64 s[56:57], s[56:57], s[58:59]
	v_add_u32_e32 v15, 0x12c, v15
	v_mov_b32_e32 v14, 0x12c
	v_cndmask_b32_e64 v15, v14, v15, s[56:57]
	v_lshlrev_b32_e32 v15, 2, v15
	global_load_dword v14, v15, s[12:13]
	v_mul_u32_u24_e32 v11, 0x780, v11
	v_lshl_add_u32 v11, v10, 2, v11
	s_waitcnt vmcnt(0)
	v_mul_f32_e32 v14, s52, v14
	v_mul_f32_e32 v9, s52, v9
	v_cndmask_b32_e64 v14, 0, v14, s[56:57]
	v_cndmask_b32_e64 v113, 0, v9, s[54:55]
	s_and_saveexec_b64 s[44:45], s[58:59]
	ds_write_b32 v11, v14 offset:1800
	ds_write_b32 v11, v14 offset:32520
	s_mov_b64 exec, s[44:45]
	v_lshlrev_b32_e32 v172, 3, v2
	s_lshl_b32 s35, s6, 1
	s_sub_i32 s40, 15, s35
	s_cmp_eq_u32 s4, 0
	s_cselect_b32 s41, s35, s40
	s_add_i32 s35, s35, 1
	s_sub_i32 s40, 15, s35
	s_cmp_eq_u32 s4, 0
	s_cselect_b32 s40, s35, s40
	s_mul_i32 s41, s41, 0x780
	s_mul_i32 s40, s40, 0x780
	v_add_u32_e32 v173, s41, v172
	v_add_u32_e32 v174, s40, v172
	v_min_u32_e32 v6, 32, v2
	v_lshlrev_b32_e32 v114, 3, v6
	v_add_u32_e32 v115, s41, v114
	v_add_u32_e32 v169, s40, v114
	v_cmp_lt_u32_e32 vcc, 21, v2
	v_mov_b32_e32 v6, s51
	v_mov_b32_e32 v7, s52
	s_nop 0
	v_cndmask_b32_e32 v175, v6, v7, vcc
	global_load_dwordx2 v[176:177], v172, s[22:23] offset:0
	global_load_dwordx2 v[178:179], v172, s[22:23] offset:512
	global_load_dwordx2 v[180:181], v172, s[22:23] offset:1024
	global_load_dwordx2 v[184:185], v172, s[46:47] offset:0
	global_load_dwordx2 v[186:187], v172, s[46:47] offset:512
	global_load_dwordx2 v[188:189], v172, s[46:47] offset:1024
	global_load_dwordx2 v[182:183], v114, s[22:23] offset:1536
	global_load_dwordx2 v[190:191], v114, s[46:47] offset:1536
	s_waitcnt vmcnt(0)
	v_mul_f32_e32 v176, s51, v176
	v_mul_f32_e32 v177, s51, v177
	v_mul_f32_e32 v178, s51, v178
	v_mul_f32_e32 v179, s51, v179
	v_mul_f32_e32 v180, v175, v180
	v_mul_f32_e32 v181, v175, v181
	v_mul_f32_e32 v182, s52, v182
	v_mul_f32_e32 v183, s52, v183
	ds_write_b64 v173, v[176:177] offset:0
	ds_write_b64 v173, v[178:179] offset:512
	ds_write_b64 v173, v[180:181] offset:1024
	ds_write_b64 v115, v[182:183] offset:1536
	v_mul_f32_e32 v184, s51, v184
	v_mul_f32_e32 v185, s51, v185
	v_mul_f32_e32 v186, s51, v186
	v_mul_f32_e32 v187, s51, v187
	v_mul_f32_e32 v188, v175, v188
	v_mul_f32_e32 v189, v175, v189
	v_mul_f32_e32 v190, s52, v190
	v_mul_f32_e32 v191, s52, v191
	ds_write_b64 v174, v[184:185] offset:0
	ds_write_b64 v174, v[186:187] offset:512
	ds_write_b64 v174, v[188:189] offset:1024
	ds_write_b64 v169, v[190:191] offset:1536
	s_movk_i32 s55, 0x7800
	v_add_u32_e32 v173, s55, v173
	v_add_u32_e32 v174, s55, v174
	v_add_u32_e32 v115, s55, v115
	v_add_u32_e32 v169, s55, v169
	s_sub_i32 s55, 0, s55
	v_add_u32_e32 v6, s53, v2
	v_cmp_gt_u32_e32 vcc, 0x96, v6
	v_cmp_gt_u32_e64 s[56:57], 16, v2
	v_cmp_gt_u32_e64 s[58:59], 19, v2
	s_and_b64 s[56:57], s[56:57], vcc
	s_and_b64 s[58:59], s[58:59], vcc
	v_mov_b32_e32 v7, 0x710
	v_lshlrev_b32_e32 v8, 2, v6
	v_add_u32_e32 v9, 0x258, v8
	v_add_u32_e32 v10, 0x4b0, v8
	v_cndmask_b32_e64 v163, v7, v8, s[56:57]
	v_cndmask_b32_e64 v164, v7, v9, s[56:57]
	v_cndmask_b32_e64 v166, v7, v10, s[58:59]
	v_subrev_u32_e32 v9, 16, v2
	v_cmp_gt_u32_e64 s[60:61], 6, v9
	v_cmp_lt_u32_e32 vcc, 2, v9
	v_mov_b32_e32 v11, 0x93
	s_nop 0
	v_cndmask_b32_e32 v10, 0, v11, vcc
	v_cndmask_b32_e64 v12, 0, 3, vcc
	v_sub_u32_e32 v13, v6, v12
	v_cmp_gt_u32_e32 vcc, 0x96, v13
	s_and_b64 s[60:61], s[60:61], vcc
	v_add_u32_e32 v13, v6, v10
	v_lshlrev_b32_e32 v13, 2, v13
	v_cndmask_b32_e64 v165, v7, v13, s[60:61]
	v_subrev_u32_e32 v9, 22, v2
	v_cmp_gt_u32_e32 vcc, 3, v9
	s_mul_i32 s35, s6, 3
	s_addk_i32 s35, 0x1c8
	v_add_lshl_u32 v9, v9, s35, 2
	s_nop 0
	v_cndmask_b32_e32 v165, v165, v9, vcc
	v_and_b32_e32 v9, 1, v3
	v_lshlrev_b32_e32 v9, 4, v9
	v_lshl_or_b32 v9, v4, 5, v9
	v_add_u32_e32 v167, 0xf000, v9
	v_and_b32_e32 v9, 0xfffffff0, v6
	v_bfe_u32 v10, v6, 1, 1
	v_lshl_or_b32 v9, v10, 3, v9
	v_bfe_u32 v10, v6, 2, 2
	v_lshl_or_b32 v9, v10, 1, v9
	v_and_b32_e32 v10, 1, v6
	v_or_b32_e32 v9, v9, v10
	v_lshlrev_b32_e32 v9, 1, v9
	v_add_u32_e32 v9, 0xf000, v9
	v_lshlrev_b32_e32 v10, 1, v2
	v_add_u32_e32 v10, 0xf300, v10
	v_cndmask_b32_e64 v168, v10, v9, s[58:59]
	s_mul_i32 s35, s4, 0x25350
	s_add_u32 s14, s14, s35
	s_addc_u32 s15, s15, 0
	s_add_u32 s18, s18, 0x25800
	s_addc_u32 s19, s19, 0
	v_lshlrev_b32_e32 v9, 2, v0
	v_mov_b32_e32 v10, s18
	v_mov_b32_e32 v11, s19
	v_mov_b32_e32 v12, s14
	v_mov_b32_e32 v13, s15
	v_cndmask_b32_e64 v9, v9, v8, s[58:59]
	v_cndmask_b32_e64 v10, v10, v12, s[58:59]
	v_cndmask_b32_e64 v11, v11, v13, s[58:59]
	v_add_co_u32_e32 v170, vcc, v10, v9
	s_nop 1
	v_addc_co_u32_e32 v171, vcc, 0, v11, vcc
	v_mov_b32_e32 v161, 0
	v_mov_b32_e32 v137, 0
	v_mov_b32_e32 v138, 0
	v_mov_b32_e32 v139, 0
	v_mov_b32_e32 v141, 0
	v_mov_b32_e32 v142, 0
	v_mov_b32_e32 v143, 0
	v_mov_b32_e32 v145, 0
	v_mov_b32_e32 v146, 0
	v_mov_b32_e32 v147, 0
	v_mov_b32_e32 v149, 0
	v_mov_b32_e32 v150, 0
	v_mov_b32_e32 v151, 0
	s_mov_b32 s26, 0
	s_waitcnt vmcnt(0) lgkmcnt(0)
	s_barrier
	ds_read_b32 v136, v163 offset:0
	ds_read_b32 v140, v164 offset:0
	ds_read_b32 v148, v165 offset:0
	ds_read_b32 v152, v166 offset:0
	v_mov_b32_e32 v144, v113
	s_waitcnt lgkmcnt(0)
.Lgru1_chunk:
	ds_read_b128 v[116:119], v167 offset:0
	ds_read_b128 v[120:123], v167 offset:128
	ds_read_b128 v[124:127], v167 offset:256
	s_waitcnt lgkmcnt(2)
	v_smfmac_f32_16x16x64_f16 v[136:139], v[116:119], v[16:23], v112
	v_smfmac_f32_16x16x64_f16 v[148:151], v[116:119], v[88:95], v112
	v_smfmac_f32_16x16x64_f16 v[140:143], v[116:119], v[40:47], v112
	v_smfmac_f32_16x16x64_f16 v[144:147], v[116:119], v[64:71], v112
	s_waitcnt lgkmcnt(1)
	v_smfmac_f32_16x16x64_f16 v[136:139], v[120:123], v[24:31], v112
	v_smfmac_f32_16x16x64_f16 v[148:151], v[120:123], v[96:103], v112
	v_smfmac_f32_16x16x64_f16 v[140:143], v[120:123], v[48:55], v112
	v_smfmac_f32_16x16x64_f16 v[144:147], v[120:123], v[72:79], v112
	s_waitcnt lgkmcnt(0)
	v_smfmac_f32_16x16x64_f16 v[136:139], v[124:127], v[32:39], v112
	v_smfmac_f32_16x16x64_f16 v[148:151], v[124:127], v[104:111], v112
	v_smfmac_f32_16x16x64_f16 v[140:143], v[124:127], v[56:63], v112
	v_smfmac_f32_16x16x64_f16 v[144:147], v[124:127], v[80:87], v112
	s_nop 8
	v_add_f32_e32 v153, v136, v137
	v_add_f32_e32 v156, v148, v149
	v_add_f32_e32 v154, v140, v141
	v_add_f32_e32 v155, v144, v145
	v_mov_b32_dpp v157, v156 row_shl:3 row_mask:0xf bank_mask:0xf bound_ctrl:1
	v_mov_b32_dpp v158, v156 row_shl:6 row_mask:0xf bank_mask:0xf bound_ctrl:1
	v_cndmask_b32_e64 v159, v156, v153, s[28:29]
	v_exp_f32_e32 v159, v159
	v_cndmask_b32_e64 v160, v157, v154, s[28:29]
	v_exp_f32_e32 v160, v160
	v_cndmask_b32_e64 v155, v158, v155, s[28:29]
	v_add_f32_e32 v159, 1.0, v159
	v_rcp_f32_e32 v159, v159
	v_add_f32_e32 v160, 1.0, v160
	v_rcp_f32_e32 v160, v160
	v_fmac_f32_e32 v152, v159, v155
	v_exp_f32_e32 v152, v152
	ds_read_b32 v136, v163 offset:1920
	ds_read_b32 v140, v164 offset:1920
	ds_read_b32 v148, v165 offset:1920
	v_mov_b32_e32 v144, v113
	v_mov_b32_e32 v137, 0
	v_mov_b32_e32 v141, 0
	v_mov_b32_e32 v145, 0
	v_mov_b32_e32 v149, 0
	v_add_f32_e32 v152, 1.0, v152
	v_rcp_f32_e32 v159, v152
	s_nop 0
	v_fma_f32 v159, v159, -2.0, 1.0
	ds_read_b32 v152, v166 offset:1920
	v_sub_f32_e32 v153, v161, v159
	v_fma_mixlo_f16 v162, v160, v153, v159
	v_fma_f32 v161, v160, v153, v159
	ds_write_b16 v168, v162 offset:384
	global_store_dword v[170:171], v161, off
	v_lshl_add_u64 v[170:171], v[170:171], 0, s[20:21]
	s_waitcnt lgkmcnt(0)
	s_barrier
	ds_read_b128 v[116:119], v167 offset:384
	ds_read_b128 v[120:123], v167 offset:512
	ds_read_b128 v[124:127], v167 offset:640
	s_waitcnt lgkmcnt(2)
	v_smfmac_f32_16x16x64_f16 v[136:139], v[116:119], v[16:23], v112
	v_smfmac_f32_16x16x64_f16 v[148:151], v[116:119], v[88:95], v112
	v_smfmac_f32_16x16x64_f16 v[140:143], v[116:119], v[40:47], v112
	v_smfmac_f32_16x16x64_f16 v[144:147], v[116:119], v[64:71], v112
	s_waitcnt lgkmcnt(1)
	v_smfmac_f32_16x16x64_f16 v[136:139], v[120:123], v[24:31], v112
	v_smfmac_f32_16x16x64_f16 v[148:151], v[120:123], v[96:103], v112
	v_smfmac_f32_16x16x64_f16 v[140:143], v[120:123], v[48:55], v112
	v_smfmac_f32_16x16x64_f16 v[144:147], v[120:123], v[72:79], v112
	s_waitcnt lgkmcnt(0)
	s_cmp_eq_u32 s26, 7
	s_cbranch_scc1 .Lgru1_nopf
	s_add_u32 s22, s22, s27
	s_addc_u32 s23, s23, s50
	s_add_u32 s46, s46, s27
	s_addc_u32 s47, s47, s50
	global_load_dwordx2 v[176:177], v172, s[22:23] offset:0
	global_load_dwordx2 v[178:179], v172, s[22:23] offset:512
	global_load_dwordx2 v[180:181], v172, s[22:23] offset:1024
	global_load_dwordx2 v[184:185], v172, s[46:47] offset:0
	global_load_dwordx2 v[186:187], v172, s[46:47] offset:512
	global_load_dwordx2 v[188:189], v172, s[46:47] offset:1024
	global_load_dwordx2 v[182:183], v114, s[22:23] offset:1536
	global_load_dwordx2 v[190:191], v114, s[46:47] offset:1536
.Lgru1_nopf:
	v_smfmac_f32_16x16x64_f16 v[136:139], v[124:127], v[32:39], v112
	v_smfmac_f32_16x16x64_f16 v[148:151], v[124:127], v[104:111], v112
	v_smfmac_f32_16x16x64_f16 v[140:143], v[124:127], v[56:63], v112
	v_smfmac_f32_16x16x64_f16 v[144:147], v[124:127], v[80:87], v112
	s_nop 8
	v_add_f32_e32 v153, v136, v137
	v_add_f32_e32 v156, v148, v149
	v_add_f32_e32 v154, v140, v141
	v_add_f32_e32 v155, v144, v145
	v_mov_b32_dpp v157, v156 row_shl:3 row_mask:0xf bank_mask:0xf bound_ctrl:1
	v_mov_b32_dpp v158, v156 row_shl:6 row_mask:0xf bank_mask:0xf bound_ctrl:1
	v_cndmask_b32_e64 v159, v156, v153, s[28:29]
	v_exp_f32_e32 v159, v159
	v_cndmask_b32_e64 v160, v157, v154, s[28:29]
	v_exp_f32_e32 v160, v160
	v_cndmask_b32_e64 v155, v158, v155, s[28:29]
	v_add_f32_e32 v159, 1.0, v159
	v_rcp_f32_e32 v159, v159
	v_add_f32_e32 v160, 1.0, v160
	v_rcp_f32_e32 v160, v160
	v_fmac_f32_e32 v152, v159, v155
	v_exp_f32_e32 v152, v152
	ds_read_b32 v136, v163 offset:3840
	ds_read_b32 v140, v164 offset:3840
	ds_read_b32 v148, v165 offset:3840
	v_mov_b32_e32 v144, v113
	v_mov_b32_e32 v137, 0
	v_mov_b32_e32 v141, 0
	v_mov_b32_e32 v145, 0
	v_mov_b32_e32 v149, 0
	v_add_f32_e32 v152, 1.0, v152
	v_rcp_f32_e32 v159, v152
	s_nop 0
	v_fma_f32 v159, v159, -2.0, 1.0
	ds_read_b32 v152, v166 offset:3840
	v_sub_f32_e32 v153, v161, v159
	v_fma_mixlo_f16 v162, v160, v153, v159
	v_fma_f32 v161, v160, v153, v159
	ds_write_b16 v168, v162 offset:0
	global_store_dword v[170:171], v161, off
	v_lshl_add_u64 v[170:171], v[170:171], 0, s[20:21]
	s_waitcnt lgkmcnt(0)
	s_barrier
	ds_read_b128 v[116:119], v167 offset:0
	ds_read_b128 v[120:123], v167 offset:128
	ds_read_b128 v[124:127], v167 offset:256
	s_waitcnt lgkmcnt(2)
	v_smfmac_f32_16x16x64_f16 v[136:139], v[116:119], v[16:23], v112
	v_smfmac_f32_16x16x64_f16 v[148:151], v[116:119], v[88:95], v112
	v_smfmac_f32_16x16x64_f16 v[140:143], v[116:119], v[40:47], v112
	v_smfmac_f32_16x16x64_f16 v[144:147], v[116:119], v[64:71], v112
	s_waitcnt lgkmcnt(1)
	v_smfmac_f32_16x16x64_f16 v[136:139], v[120:123], v[24:31], v112
	v_smfmac_f32_16x16x64_f16 v[148:151], v[120:123], v[96:103], v112
	v_smfmac_f32_16x16x64_f16 v[140:143], v[120:123], v[48:55], v112
	v_smfmac_f32_16x16x64_f16 v[144:147], v[120:123], v[72:79], v112
	s_waitcnt lgkmcnt(0)
	v_smfmac_f32_16x16x64_f16 v[136:139], v[124:127], v[32:39], v112
	v_smfmac_f32_16x16x64_f16 v[148:151], v[124:127], v[104:111], v112
	v_smfmac_f32_16x16x64_f16 v[140:143], v[124:127], v[56:63], v112
	v_smfmac_f32_16x16x64_f16 v[144:147], v[124:127], v[80:87], v112
	s_nop 8
	v_add_f32_e32 v153, v136, v137
	v_add_f32_e32 v156, v148, v149
	v_add_f32_e32 v154, v140, v141
	v_add_f32_e32 v155, v144, v145
	v_mov_b32_dpp v157, v156 row_shl:3 row_mask:0xf bank_mask:0xf bound_ctrl:1
	v_mov_b32_dpp v158, v156 row_shl:6 row_mask:0xf bank_mask:0xf bound_ctrl:1
	v_cndmask_b32_e64 v159, v156, v153, s[28:29]
	v_exp_f32_e32 v159, v159
	v_cndmask_b32_e64 v160, v157, v154, s[28:29]
	v_exp_f32_e32 v160, v160
	v_cndmask_b32_e64 v155, v158, v155, s[28:29]
	v_add_f32_e32 v159, 1.0, v159
	v_rcp_f32_e32 v159, v159
	v_add_f32_e32 v160, 1.0, v160
	v_rcp_f32_e32 v160, v160
	v_fmac_f32_e32 v152, v159, v155
	v_exp_f32_e32 v152, v152
	ds_read_b32 v136, v163 offset:5760
	ds_read_b32 v140, v164 offset:5760
	ds_read_b32 v148, v165 offset:5760
	v_mov_b32_e32 v144, v113
	v_mov_b32_e32 v137, 0
	v_mov_b32_e32 v141, 0
	v_mov_b32_e32 v145, 0
	v_mov_b32_e32 v149, 0
	v_add_f32_e32 v152, 1.0, v152
	v_rcp_f32_e32 v159, v152
	s_nop 0
	v_fma_f32 v159, v159, -2.0, 1.0
	ds_read_b32 v152, v166 offset:5760
	v_sub_f32_e32 v153, v161, v159
	v_fma_mixlo_f16 v162, v160, v153, v159
	v_fma_f32 v161, v160, v153, v159
	ds_write_b16 v168, v162 offset:384
	global_store_dword v[170:171], v161, off
	v_lshl_add_u64 v[170:171], v[170:171], 0, s[20:21]
	s_waitcnt lgkmcnt(0)
	s_barrier
	ds_read_b128 v[116:119], v167 offset:384
	ds_read_b128 v[120:123], v167 offset:512
	ds_read_b128 v[124:127], v167 offset:640
	s_waitcnt lgkmcnt(2)
	v_smfmac_f32_16x16x64_f16 v[136:139], v[116:119], v[16:23], v112
	v_smfmac_f32_16x16x64_f16 v[148:151], v[116:119], v[88:95], v112
	v_smfmac_f32_16x16x64_f16 v[140:143], v[116:119], v[40:47], v112
	v_smfmac_f32_16x16x64_f16 v[144:147], v[116:119], v[64:71], v112
	s_waitcnt lgkmcnt(1)
	v_smfmac_f32_16x16x64_f16 v[136:139], v[120:123], v[24:31], v112
	v_smfmac_f32_16x16x64_f16 v[148:151], v[120:123], v[96:103], v112
	v_smfmac_f32_16x16x64_f16 v[140:143], v[120:123], v[48:55], v112
	v_smfmac_f32_16x16x64_f16 v[144:147], v[120:123], v[72:79], v112
	s_waitcnt lgkmcnt(0)
	v_smfmac_f32_16x16x64_f16 v[136:139], v[124:127], v[32:39], v112
	v_smfmac_f32_16x16x64_f16 v[148:151], v[124:127], v[104:111], v112
	v_smfmac_f32_16x16x64_f16 v[140:143], v[124:127], v[56:63], v112
	v_smfmac_f32_16x16x64_f16 v[144:147], v[124:127], v[80:87], v112
	s_nop 8
	v_add_f32_e32 v153, v136, v137
	v_add_f32_e32 v156, v148, v149
	v_add_f32_e32 v154, v140, v141
	v_add_f32_e32 v155, v144, v145
	v_mov_b32_dpp v157, v156 row_shl:3 row_mask:0xf bank_mask:0xf bound_ctrl:1
	v_mov_b32_dpp v158, v156 row_shl:6 row_mask:0xf bank_mask:0xf bound_ctrl:1
	v_cndmask_b32_e64 v159, v156, v153, s[28:29]
	v_exp_f32_e32 v159, v159
	v_cndmask_b32_e64 v160, v157, v154, s[28:29]
	v_exp_f32_e32 v160, v160
	v_cndmask_b32_e64 v155, v158, v155, s[28:29]
	v_add_f32_e32 v159, 1.0, v159
	v_rcp_f32_e32 v159, v159
	v_add_f32_e32 v160, 1.0, v160
	v_rcp_f32_e32 v160, v160
	v_fmac_f32_e32 v152, v159, v155
	v_exp_f32_e32 v152, v152
	ds_read_b32 v136, v163 offset:7680
	ds_read_b32 v140, v164 offset:7680
	ds_read_b32 v148, v165 offset:7680
	v_mov_b32_e32 v144, v113
	v_mov_b32_e32 v137, 0
	v_mov_b32_e32 v141, 0
	v_mov_b32_e32 v145, 0
	v_mov_b32_e32 v149, 0
	v_add_f32_e32 v152, 1.0, v152
	v_rcp_f32_e32 v159, v152
	s_nop 0
	v_fma_f32 v159, v159, -2.0, 1.0
	ds_read_b32 v152, v166 offset:7680
	v_sub_f32_e32 v153, v161, v159
	v_fma_mixlo_f16 v162, v160, v153, v159
	v_fma_f32 v161, v160, v153, v159
	ds_write_b16 v168, v162 offset:0
	global_store_dword v[170:171], v161, off
	v_lshl_add_u64 v[170:171], v[170:171], 0, s[20:21]
	s_waitcnt lgkmcnt(0)
	s_barrier
	ds_read_b128 v[116:119], v167 offset:0
	ds_read_b128 v[120:123], v167 offset:128
	ds_read_b128 v[124:127], v167 offset:256
	s_waitcnt lgkmcnt(2)
	v_smfmac_f32_16x16x64_f16 v[136:139], v[116:119], v[16:23], v112
	v_smfmac_f32_16x16x64_f16 v[148:151], v[116:119], v[88:95], v112
	v_smfmac_f32_16x16x64_f16 v[140:143], v[116:119], v[40:47], v112
	v_smfmac_f32_16x16x64_f16 v[144:147], v[116:119], v[64:71], v112
	s_waitcnt lgkmcnt(1)
	v_smfmac_f32_16x16x64_f16 v[136:139], v[120:123], v[24:31], v112
	v_smfmac_f32_16x16x64_f16 v[148:151], v[120:123], v[96:103], v112
	v_smfmac_f32_16x16x64_f16 v[140:143], v[120:123], v[48:55], v112
	v_smfmac_f32_16x16x64_f16 v[144:147], v[120:123], v[72:79], v112
	s_waitcnt lgkmcnt(0)
	v_smfmac_f32_16x16x64_f16 v[136:139], v[124:127], v[32:39], v112
	v_smfmac_f32_16x16x64_f16 v[148:151], v[124:127], v[104:111], v112
	v_smfmac_f32_16x16x64_f16 v[140:143], v[124:127], v[56:63], v112
	v_smfmac_f32_16x16x64_f16 v[144:147], v[124:127], v[80:87], v112
	s_nop 8
	v_add_f32_e32 v153, v136, v137
	v_add_f32_e32 v156, v148, v149
	v_add_f32_e32 v154, v140, v141
	v_add_f32_e32 v155, v144, v145
	v_mov_b32_dpp v157, v156 row_shl:3 row_mask:0xf bank_mask:0xf bound_ctrl:1
	v_mov_b32_dpp v158, v156 row_shl:6 row_mask:0xf bank_mask:0xf bound_ctrl:1
	v_cndmask_b32_e64 v159, v156, v153, s[28:29]
	v_exp_f32_e32 v159, v159
	v_cndmask_b32_e64 v160, v157, v154, s[28:29]
	v_exp_f32_e32 v160, v160
	v_cndmask_b32_e64 v155, v158, v155, s[28:29]
	v_add_f32_e32 v159, 1.0, v159
	v_rcp_f32_e32 v159, v159
	v_add_f32_e32 v160, 1.0, v160
	v_rcp_f32_e32 v160, v160
	v_fmac_f32_e32 v152, v159, v155
	v_exp_f32_e32 v152, v152
	ds_read_b32 v136, v163 offset:9600
	ds_read_b32 v140, v164 offset:9600
	ds_read_b32 v148, v165 offset:9600
	v_mov_b32_e32 v144, v113
	v_mov_b32_e32 v137, 0
	v_mov_b32_e32 v141, 0
	v_mov_b32_e32 v145, 0
	v_mov_b32_e32 v149, 0
	v_add_f32_e32 v152, 1.0, v152
	v_rcp_f32_e32 v159, v152
	s_nop 0
	v_fma_f32 v159, v159, -2.0, 1.0
	ds_read_b32 v152, v166 offset:9600
	v_sub_f32_e32 v153, v161, v159
	v_fma_mixlo_f16 v162, v160, v153, v159
	v_fma_f32 v161, v160, v153, v159
	ds_write_b16 v168, v162 offset:384
	global_store_dword v[170:171], v161, off
	v_lshl_add_u64 v[170:171], v[170:171], 0, s[20:21]
	s_waitcnt lgkmcnt(0)
	s_barrier
	ds_read_b128 v[116:119], v167 offset:384
	ds_read_b128 v[120:123], v167 offset:512
	ds_read_b128 v[124:127], v167 offset:640
	s_waitcnt lgkmcnt(2)
	v_smfmac_f32_16x16x64_f16 v[136:139], v[116:119], v[16:23], v112
	v_smfmac_f32_16x16x64_f16 v[148:151], v[116:119], v[88:95], v112
	v_smfmac_f32_16x16x64_f16 v[140:143], v[116:119], v[40:47], v112
	v_smfmac_f32_16x16x64_f16 v[144:147], v[116:119], v[64:71], v112
	s_waitcnt lgkmcnt(1)
	v_smfmac_f32_16x16x64_f16 v[136:139], v[120:123], v[24:31], v112
	v_smfmac_f32_16x16x64_f16 v[148:151], v[120:123], v[96:103], v112
	v_smfmac_f32_16x16x64_f16 v[140:143], v[120:123], v[48:55], v112
	v_smfmac_f32_16x16x64_f16 v[144:147], v[120:123], v[72:79], v112
	s_waitcnt lgkmcnt(0)
	v_smfmac_f32_16x16x64_f16 v[136:139], v[124:127], v[32:39], v112
	v_smfmac_f32_16x16x64_f16 v[148:151], v[124:127], v[104:111], v112
	v_smfmac_f32_16x16x64_f16 v[140:143], v[124:127], v[56:63], v112
	v_smfmac_f32_16x16x64_f16 v[144:147], v[124:127], v[80:87], v112
	s_nop 8
	v_add_f32_e32 v153, v136, v137
	v_add_f32_e32 v156, v148, v149
	v_add_f32_e32 v154, v140, v141
	v_add_f32_e32 v155, v144, v145
	v_mov_b32_dpp v157, v156 row_shl:3 row_mask:0xf bank_mask:0xf bound_ctrl:1
	v_mov_b32_dpp v158, v156 row_shl:6 row_mask:0xf bank_mask:0xf bound_ctrl:1
	v_cndmask_b32_e64 v159, v156, v153, s[28:29]
	v_exp_f32_e32 v159, v159
	v_cndmask_b32_e64 v160, v157, v154, s[28:29]
	v_exp_f32_e32 v160, v160
	v_cndmask_b32_e64 v155, v158, v155, s[28:29]
	v_add_f32_e32 v159, 1.0, v159
	v_rcp_f32_e32 v159, v159
	v_add_f32_e32 v160, 1.0, v160
	v_rcp_f32_e32 v160, v160
	v_fmac_f32_e32 v152, v159, v155
	v_exp_f32_e32 v152, v152
	ds_read_b32 v136, v163 offset:11520
	ds_read_b32 v140, v164 offset:11520
	ds_read_b32 v148, v165 offset:11520
	v_mov_b32_e32 v144, v113
	v_mov_b32_e32 v137, 0
	v_mov_b32_e32 v141, 0
	v_mov_b32_e32 v145, 0
	v_mov_b32_e32 v149, 0
	v_add_f32_e32 v152, 1.0, v152
	v_rcp_f32_e32 v159, v152
	s_nop 0
	v_fma_f32 v159, v159, -2.0, 1.0
	ds_read_b32 v152, v166 offset:11520
	v_sub_f32_e32 v153, v161, v159
	v_fma_mixlo_f16 v162, v160, v153, v159
	v_fma_f32 v161, v160, v153, v159
	ds_write_b16 v168, v162 offset:0
	global_store_dword v[170:171], v161, off
	v_lshl_add_u64 v[170:171], v[170:171], 0, s[20:21]
	s_waitcnt lgkmcnt(0)
	s_barrier
	ds_read_b128 v[116:119], v167 offset:0
	ds_read_b128 v[120:123], v167 offset:128
	ds_read_b128 v[124:127], v167 offset:256
	s_waitcnt lgkmcnt(2)
	v_smfmac_f32_16x16x64_f16 v[136:139], v[116:119], v[16:23], v112
	v_smfmac_f32_16x16x64_f16 v[148:151], v[116:119], v[88:95], v112
	v_smfmac_f32_16x16x64_f16 v[140:143], v[116:119], v[40:47], v112
	v_smfmac_f32_16x16x64_f16 v[144:147], v[116:119], v[64:71], v112
	s_waitcnt lgkmcnt(1)
	v_smfmac_f32_16x16x64_f16 v[136:139], v[120:123], v[24:31], v112
	v_smfmac_f32_16x16x64_f16 v[148:151], v[120:123], v[96:103], v112
	v_smfmac_f32_16x16x64_f16 v[140:143], v[120:123], v[48:55], v112
	v_smfmac_f32_16x16x64_f16 v[144:147], v[120:123], v[72:79], v112
	s_waitcnt lgkmcnt(0)
	v_smfmac_f32_16x16x64_f16 v[136:139], v[124:127], v[32:39], v112
	v_smfmac_f32_16x16x64_f16 v[148:151], v[124:127], v[104:111], v112
	v_smfmac_f32_16x16x64_f16 v[140:143], v[124:127], v[56:63], v112
	v_smfmac_f32_16x16x64_f16 v[144:147], v[124:127], v[80:87], v112
	s_nop 8
	v_add_f32_e32 v153, v136, v137
	v_add_f32_e32 v156, v148, v149
	v_add_f32_e32 v154, v140, v141
	v_add_f32_e32 v155, v144, v145
	v_mov_b32_dpp v157, v156 row_shl:3 row_mask:0xf bank_mask:0xf bound_ctrl:1
	v_mov_b32_dpp v158, v156 row_shl:6 row_mask:0xf bank_mask:0xf bound_ctrl:1
	v_cndmask_b32_e64 v159, v156, v153, s[28:29]
	v_exp_f32_e32 v159, v159
	v_cndmask_b32_e64 v160, v157, v154, s[28:29]
	v_exp_f32_e32 v160, v160
	v_cndmask_b32_e64 v155, v158, v155, s[28:29]
	v_add_f32_e32 v159, 1.0, v159
	v_rcp_f32_e32 v159, v159
	v_add_f32_e32 v160, 1.0, v160
	v_rcp_f32_e32 v160, v160
	v_fmac_f32_e32 v152, v159, v155
	v_exp_f32_e32 v152, v152
	ds_read_b32 v136, v163 offset:13440
	ds_read_b32 v140, v164 offset:13440
	ds_read_b32 v148, v165 offset:13440
	v_mov_b32_e32 v144, v113
	v_mov_b32_e32 v137, 0
	v_mov_b32_e32 v141, 0
	v_mov_b32_e32 v145, 0
	v_mov_b32_e32 v149, 0
	v_add_f32_e32 v152, 1.0, v152
	v_rcp_f32_e32 v159, v152
	s_nop 0
	v_fma_f32 v159, v159, -2.0, 1.0
	ds_read_b32 v152, v166 offset:13440
	v_sub_f32_e32 v153, v161, v159
	v_fma_mixlo_f16 v162, v160, v153, v159
	v_fma_f32 v161, v160, v153, v159
	ds_write_b16 v168, v162 offset:384
	global_store_dword v[170:171], v161, off
	v_lshl_add_u64 v[170:171], v[170:171], 0, s[20:21]
	s_waitcnt lgkmcnt(0)
	s_barrier
	ds_read_b128 v[116:119], v167 offset:384
	ds_read_b128 v[120:123], v167 offset:512
	ds_read_b128 v[124:127], v167 offset:640
	s_waitcnt lgkmcnt(2)
	v_smfmac_f32_16x16x64_f16 v[136:139], v[116:119], v[16:23], v112
	v_smfmac_f32_16x16x64_f16 v[148:151], v[116:119], v[88:95], v112
	v_smfmac_f32_16x16x64_f16 v[140:143], v[116:119], v[40:47], v112
	v_smfmac_f32_16x16x64_f16 v[144:147], v[116:119], v[64:71], v112
	s_waitcnt lgkmcnt(1)
	v_smfmac_f32_16x16x64_f16 v[136:139], v[120:123], v[24:31], v112
	v_smfmac_f32_16x16x64_f16 v[148:151], v[120:123], v[96:103], v112
	v_smfmac_f32_16x16x64_f16 v[140:143], v[120:123], v[48:55], v112
	v_smfmac_f32_16x16x64_f16 v[144:147], v[120:123], v[72:79], v112
	s_waitcnt lgkmcnt(0)
	v_smfmac_f32_16x16x64_f16 v[136:139], v[124:127], v[32:39], v112
	v_smfmac_f32_16x16x64_f16 v[148:151], v[124:127], v[104:111], v112
	v_smfmac_f32_16x16x64_f16 v[140:143], v[124:127], v[56:63], v112
	v_smfmac_f32_16x16x64_f16 v[144:147], v[124:127], v[80:87], v112
	s_nop 8
	v_add_f32_e32 v153, v136, v137
	v_add_f32_e32 v156, v148, v149
	v_add_f32_e32 v154, v140, v141
	v_add_f32_e32 v155, v144, v145
	v_mov_b32_dpp v157, v156 row_shl:3 row_mask:0xf bank_mask:0xf bound_ctrl:1
	v_mov_b32_dpp v158, v156 row_shl:6 row_mask:0xf bank_mask:0xf bound_ctrl:1
	v_cndmask_b32_e64 v159, v156, v153, s[28:29]
	v_exp_f32_e32 v159, v159
	v_cndmask_b32_e64 v160, v157, v154, s[28:29]
	v_exp_f32_e32 v160, v160
	v_cndmask_b32_e64 v155, v158, v155, s[28:29]
	v_add_f32_e32 v159, 1.0, v159
	v_rcp_f32_e32 v159, v159
	v_add_f32_e32 v160, 1.0, v160
	v_rcp_f32_e32 v160, v160
	v_fmac_f32_e32 v152, v159, v155
	v_exp_f32_e32 v152, v152
	ds_read_b32 v136, v163 offset:15360
	ds_read_b32 v140, v164 offset:15360
	ds_read_b32 v148, v165 offset:15360
	v_mov_b32_e32 v144, v113
	v_mov_b32_e32 v137, 0
	v_mov_b32_e32 v141, 0
	v_mov_b32_e32 v145, 0
	v_mov_b32_e32 v149, 0
	v_add_f32_e32 v152, 1.0, v152
	v_rcp_f32_e32 v159, v152
	s_nop 0
	v_fma_f32 v159, v159, -2.0, 1.0
	ds_read_b32 v152, v166 offset:15360
	v_sub_f32_e32 v153, v161, v159
	v_fma_mixlo_f16 v162, v160, v153, v159
	v_fma_f32 v161, v160, v153, v159
	ds_write_b16 v168, v162 offset:0
	global_store_dword v[170:171], v161, off
	v_lshl_add_u64 v[170:171], v[170:171], 0, s[20:21]
	s_waitcnt lgkmcnt(0)
	s_barrier
	ds_read_b128 v[116:119], v167 offset:0
	ds_read_b128 v[120:123], v167 offset:128
	ds_read_b128 v[124:127], v167 offset:256
	s_waitcnt lgkmcnt(2)
	v_smfmac_f32_16x16x64_f16 v[136:139], v[116:119], v[16:23], v112
	v_smfmac_f32_16x16x64_f16 v[148:151], v[116:119], v[88:95], v112
	v_smfmac_f32_16x16x64_f16 v[140:143], v[116:119], v[40:47], v112
	v_smfmac_f32_16x16x64_f16 v[144:147], v[116:119], v[64:71], v112
	s_waitcnt lgkmcnt(1)
	v_smfmac_f32_16x16x64_f16 v[136:139], v[120:123], v[24:31], v112
	v_smfmac_f32_16x16x64_f16 v[148:151], v[120:123], v[96:103], v112
	v_smfmac_f32_16x16x64_f16 v[140:143], v[120:123], v[48:55], v112
	v_smfmac_f32_16x16x64_f16 v[144:147], v[120:123], v[72:79], v112
	s_waitcnt lgkmcnt(0)
	v_smfmac_f32_16x16x64_f16 v[136:139], v[124:127], v[32:39], v112
	v_smfmac_f32_16x16x64_f16 v[148:151], v[124:127], v[104:111], v112
	v_smfmac_f32_16x16x64_f16 v[140:143], v[124:127], v[56:63], v112
	v_smfmac_f32_16x16x64_f16 v[144:147], v[124:127], v[80:87], v112
	s_nop 8
	v_add_f32_e32 v153, v136, v137
	v_add_f32_e32 v156, v148, v149
	v_add_f32_e32 v154, v140, v141
	v_add_f32_e32 v155, v144, v145
	v_mov_b32_dpp v157, v156 row_shl:3 row_mask:0xf bank_mask:0xf bound_ctrl:1
	v_mov_b32_dpp v158, v156 row_shl:6 row_mask:0xf bank_mask:0xf bound_ctrl:1
	v_cndmask_b32_e64 v159, v156, v153, s[28:29]
	v_exp_f32_e32 v159, v159
	v_cndmask_b32_e64 v160, v157, v154, s[28:29]
	v_exp_f32_e32 v160, v160
	v_cndmask_b32_e64 v155, v158, v155, s[28:29]
	v_add_f32_e32 v159, 1.0, v159
	v_rcp_f32_e32 v159, v159
	v_add_f32_e32 v160, 1.0, v160
	v_rcp_f32_e32 v160, v160
	v_fmac_f32_e32 v152, v159, v155
	v_exp_f32_e32 v152, v152
	ds_read_b32 v136, v163 offset:17280
	ds_read_b32 v140, v164 offset:17280
	ds_read_b32 v148, v165 offset:17280
	v_mov_b32_e32 v144, v113
	v_mov_b32_e32 v137, 0
	v_mov_b32_e32 v141, 0
	v_mov_b32_e32 v145, 0
	v_mov_b32_e32 v149, 0
	v_add_f32_e32 v152, 1.0, v152
	v_rcp_f32_e32 v159, v152
	s_nop 0
	v_fma_f32 v159, v159, -2.0, 1.0
	ds_read_b32 v152, v166 offset:17280
	v_sub_f32_e32 v153, v161, v159
	v_fma_mixlo_f16 v162, v160, v153, v159
	v_fma_f32 v161, v160, v153, v159
	ds_write_b16 v168, v162 offset:384
	global_store_dword v[170:171], v161, off
	v_lshl_add_u64 v[170:171], v[170:171], 0, s[20:21]
	s_waitcnt lgkmcnt(0)
	s_barrier
	ds_read_b128 v[116:119], v167 offset:384
	ds_read_b128 v[120:123], v167 offset:512
	ds_read_b128 v[124:127], v167 offset:640
	s_waitcnt lgkmcnt(2)
	v_smfmac_f32_16x16x64_f16 v[136:139], v[116:119], v[16:23], v112
	v_smfmac_f32_16x16x64_f16 v[148:151], v[116:119], v[88:95], v112
	v_smfmac_f32_16x16x64_f16 v[140:143], v[116:119], v[40:47], v112
	v_smfmac_f32_16x16x64_f16 v[144:147], v[116:119], v[64:71], v112
	s_waitcnt lgkmcnt(1)
	v_smfmac_f32_16x16x64_f16 v[136:139], v[120:123], v[24:31], v112
	v_smfmac_f32_16x16x64_f16 v[148:151], v[120:123], v[96:103], v112
	v_smfmac_f32_16x16x64_f16 v[140:143], v[120:123], v[48:55], v112
	v_smfmac_f32_16x16x64_f16 v[144:147], v[120:123], v[72:79], v112
	s_waitcnt lgkmcnt(0)
	s_cmp_eq_u32 s26, 7
	s_cbranch_scc1 .Lgru1_nost0
	s_waitcnt vmcnt(4)
	v_mul_f32_e32 v176, s51, v176
	v_mul_f32_e32 v177, s51, v177
	v_mul_f32_e32 v178, s51, v178
	v_mul_f32_e32 v179, s51, v179
	v_mul_f32_e32 v180, v175, v180
	v_mul_f32_e32 v181, v175, v181
	v_mul_f32_e32 v182, s52, v182
	v_mul_f32_e32 v183, s52, v183
	ds_write_b64 v173, v[176:177] offset:0
	ds_write_b64 v173, v[178:179] offset:512
	ds_write_b64 v173, v[180:181] offset:1024
	ds_write_b64 v115, v[182:183] offset:1536
.Lgru1_nost0:
	v_smfmac_f32_16x16x64_f16 v[136:139], v[124:127], v[32:39], v112
	v_smfmac_f32_16x16x64_f16 v[148:151], v[124:127], v[104:111], v112
	v_smfmac_f32_16x16x64_f16 v[140:143], v[124:127], v[56:63], v112
	v_smfmac_f32_16x16x64_f16 v[144:147], v[124:127], v[80:87], v112
	s_nop 8
	v_add_f32_e32 v153, v136, v137
	v_add_f32_e32 v156, v148, v149
	v_add_f32_e32 v154, v140, v141
	v_add_f32_e32 v155, v144, v145
	v_mov_b32_dpp v157, v156 row_shl:3 row_mask:0xf bank_mask:0xf bound_ctrl:1
	v_mov_b32_dpp v158, v156 row_shl:6 row_mask:0xf bank_mask:0xf bound_ctrl:1
	v_cndmask_b32_e64 v159, v156, v153, s[28:29]
	v_exp_f32_e32 v159, v159
	v_cndmask_b32_e64 v160, v157, v154, s[28:29]
	v_exp_f32_e32 v160, v160
	v_cndmask_b32_e64 v155, v158, v155, s[28:29]
	v_add_f32_e32 v159, 1.0, v159
	v_rcp_f32_e32 v159, v159
	v_add_f32_e32 v160, 1.0, v160
	v_rcp_f32_e32 v160, v160
	v_fmac_f32_e32 v152, v159, v155
	v_exp_f32_e32 v152, v152
	ds_read_b32 v136, v163 offset:19200
	ds_read_b32 v140, v164 offset:19200
	ds_read_b32 v148, v165 offset:19200
	v_mov_b32_e32 v144, v113
	v_mov_b32_e32 v137, 0
	v_mov_b32_e32 v141, 0
	v_mov_b32_e32 v145, 0
	v_mov_b32_e32 v149, 0
	v_add_f32_e32 v152, 1.0, v152
	v_rcp_f32_e32 v159, v152
	s_nop 0
	v_fma_f32 v159, v159, -2.0, 1.0
	ds_read_b32 v152, v166 offset:19200
	v_sub_f32_e32 v153, v161, v159
	v_fma_mixlo_f16 v162, v160, v153, v159
	v_fma_f32 v161, v160, v153, v159
	ds_write_b16 v168, v162 offset:0
	global_store_dword v[170:171], v161, off
	v_lshl_add_u64 v[170:171], v[170:171], 0, s[20:21]
	s_waitcnt lgkmcnt(0)
	s_barrier
	ds_read_b128 v[116:119], v167 offset:0
	ds_read_b128 v[120:123], v167 offset:128
	ds_read_b128 v[124:127], v167 offset:256
	s_waitcnt lgkmcnt(2)
	v_smfmac_f32_16x16x64_f16 v[136:139], v[116:119], v[16:23], v112
	v_smfmac_f32_16x16x64_f16 v[148:151], v[116:119], v[88:95], v112
	v_smfmac_f32_16x16x64_f16 v[140:143], v[116:119], v[40:47], v112
	v_smfmac_f32_16x16x64_f16 v[144:147], v[116:119], v[64:71], v112
	s_waitcnt lgkmcnt(1)
	v_smfmac_f32_16x16x64_f16 v[136:139], v[120:123], v[24:31], v112
	v_smfmac_f32_16x16x64_f16 v[148:151], v[120:123], v[96:103], v112
	v_smfmac_f32_16x16x64_f16 v[140:143], v[120:123], v[48:55], v112
	v_smfmac_f32_16x16x64_f16 v[144:147], v[120:123], v[72:79], v112
	s_waitcnt lgkmcnt(0)
	v_smfmac_f32_16x16x64_f16 v[136:139], v[124:127], v[32:39], v112
	v_smfmac_f32_16x16x64_f16 v[148:151], v[124:127], v[104:111], v112
	v_smfmac_f32_16x16x64_f16 v[140:143], v[124:127], v[56:63], v112
	v_smfmac_f32_16x16x64_f16 v[144:147], v[124:127], v[80:87], v112
	s_nop 8
	v_add_f32_e32 v153, v136, v137
	v_add_f32_e32 v156, v148, v149
	v_add_f32_e32 v154, v140, v141
	v_add_f32_e32 v155, v144, v145
	v_mov_b32_dpp v157, v156 row_shl:3 row_mask:0xf bank_mask:0xf bound_ctrl:1
	v_mov_b32_dpp v158, v156 row_shl:6 row_mask:0xf bank_mask:0xf bound_ctrl:1
	v_cndmask_b32_e64 v159, v156, v153, s[28:29]
	v_exp_f32_e32 v159, v159
	v_cndmask_b32_e64 v160, v157, v154, s[28:29]
	v_exp_f32_e32 v160, v160
	v_cndmask_b32_e64 v155, v158, v155, s[28:29]
	v_add_f32_e32 v159, 1.0, v159
	v_rcp_f32_e32 v159, v159
	v_add_f32_e32 v160, 1.0, v160
	v_rcp_f32_e32 v160, v160
	v_fmac_f32_e32 v152, v159, v155
	v_exp_f32_e32 v152, v152
	ds_read_b32 v136, v163 offset:21120
	ds_read_b32 v140, v164 offset:21120
	ds_read_b32 v148, v165 offset:21120
	v_mov_b32_e32 v144, v113
	v_mov_b32_e32 v137, 0
	v_mov_b32_e32 v141, 0
	v_mov_b32_e32 v145, 0
	v_mov_b32_e32 v149, 0
	v_add_f32_e32 v152, 1.0, v152
	v_rcp_f32_e32 v159, v152
	s_nop 0
	v_fma_f32 v159, v159, -2.0, 1.0
	ds_read_b32 v152, v166 offset:21120
	v_sub_f32_e32 v153, v161, v159
	v_fma_mixlo_f16 v162, v160, v153, v159
	v_fma_f32 v161, v160, v153, v159
	ds_write_b16 v168, v162 offset:384
	global_store_dword v[170:171], v161, off
	v_lshl_add_u64 v[170:171], v[170:171], 0, s[20:21]
	s_waitcnt lgkmcnt(0)
	s_barrier
	ds_read_b128 v[116:119], v167 offset:384
	ds_read_b128 v[120:123], v167 offset:512
	ds_read_b128 v[124:127], v167 offset:640
	s_waitcnt lgkmcnt(2)
	v_smfmac_f32_16x16x64_f16 v[136:139], v[116:119], v[16:23], v112
	v_smfmac_f32_16x16x64_f16 v[148:151], v[116:119], v[88:95], v112
	v_smfmac_f32_16x16x64_f16 v[140:143], v[116:119], v[40:47], v112
	v_smfmac_f32_16x16x64_f16 v[144:147], v[116:119], v[64:71], v112
	s_waitcnt lgkmcnt(1)
	v_smfmac_f32_16x16x64_f16 v[136:139], v[120:123], v[24:31], v112
	v_smfmac_f32_16x16x64_f16 v[148:151], v[120:123], v[96:103], v112
	v_smfmac_f32_16x16x64_f16 v[140:143], v[120:123], v[48:55], v112
	v_smfmac_f32_16x16x64_f16 v[144:147], v[120:123], v[72:79], v112
	s_waitcnt lgkmcnt(0)
	s_cmp_eq_u32 s26, 7
	s_cbranch_scc1 .Lgru1_nost1
	s_waitcnt vmcnt(4)
	v_mul_f32_e32 v184, s51, v184
	v_mul_f32_e32 v185, s51, v185
	v_mul_f32_e32 v186, s51, v186
	v_mul_f32_e32 v187, s51, v187
	v_mul_f32_e32 v188, v175, v188
	v_mul_f32_e32 v189, v175, v189
	v_mul_f32_e32 v190, s52, v190
	v_mul_f32_e32 v191, s52, v191
	ds_write_b64 v174, v[184:185] offset:0
	ds_write_b64 v174, v[186:187] offset:512
	ds_write_b64 v174, v[188:189] offset:1024
	ds_write_b64 v169, v[190:191] offset:1536
.Lgru1_nost1:
	v_smfmac_f32_16x16x64_f16 v[136:139], v[124:127], v[32:39], v112
	v_smfmac_f32_16x16x64_f16 v[148:151], v[124:127], v[104:111], v112
	v_smfmac_f32_16x16x64_f16 v[140:143], v[124:127], v[56:63], v112
	v_smfmac_f32_16x16x64_f16 v[144:147], v[124:127], v[80:87], v112
	s_nop 8
	v_add_f32_e32 v153, v136, v137
	v_add_f32_e32 v156, v148, v149
	v_add_f32_e32 v154, v140, v141
	v_add_f32_e32 v155, v144, v145
	v_mov_b32_dpp v157, v156 row_shl:3 row_mask:0xf bank_mask:0xf bound_ctrl:1
	v_mov_b32_dpp v158, v156 row_shl:6 row_mask:0xf bank_mask:0xf bound_ctrl:1
	v_cndmask_b32_e64 v159, v156, v153, s[28:29]
	v_exp_f32_e32 v159, v159
	v_cndmask_b32_e64 v160, v157, v154, s[28:29]
	v_exp_f32_e32 v160, v160
	v_cndmask_b32_e64 v155, v158, v155, s[28:29]
	v_add_f32_e32 v159, 1.0, v159
	v_rcp_f32_e32 v159, v159
	v_add_f32_e32 v160, 1.0, v160
	v_rcp_f32_e32 v160, v160
	v_fmac_f32_e32 v152, v159, v155
	v_exp_f32_e32 v152, v152
	ds_read_b32 v136, v163 offset:23040
	ds_read_b32 v140, v164 offset:23040
	ds_read_b32 v148, v165 offset:23040
	v_mov_b32_e32 v144, v113
	v_mov_b32_e32 v137, 0
	v_mov_b32_e32 v141, 0
	v_mov_b32_e32 v145, 0
	v_mov_b32_e32 v149, 0
	v_add_f32_e32 v152, 1.0, v152
	v_rcp_f32_e32 v159, v152
	s_nop 0
	v_fma_f32 v159, v159, -2.0, 1.0
	ds_read_b32 v152, v166 offset:23040
	v_sub_f32_e32 v153, v161, v159
	v_fma_mixlo_f16 v162, v160, v153, v159
	v_fma_f32 v161, v160, v153, v159
	ds_write_b16 v168, v162 offset:0
	global_store_dword v[170:171], v161, off
	v_lshl_add_u64 v[170:171], v[170:171], 0, s[20:21]
	s_waitcnt lgkmcnt(0)
	s_barrier
	ds_read_b128 v[116:119], v167 offset:0
	ds_read_b128 v[120:123], v167 offset:128
	ds_read_b128 v[124:127], v167 offset:256
	s_waitcnt lgkmcnt(2)
	v_smfmac_f32_16x16x64_f16 v[136:139], v[116:119], v[16:23], v112
	v_smfmac_f32_16x16x64_f16 v[148:151], v[116:119], v[88:95], v112
	v_smfmac_f32_16x16x64_f16 v[140:143], v[116:119], v[40:47], v112
	v_smfmac_f32_16x16x64_f16 v[144:147], v[116:119], v[64:71], v112
	s_waitcnt lgkmcnt(1)
	v_smfmac_f32_16x16x64_f16 v[136:139], v[120:123], v[24:31], v112
	v_smfmac_f32_16x16x64_f16 v[148:151], v[120:123], v[96:103], v112
	v_smfmac_f32_16x16x64_f16 v[140:143], v[120:123], v[48:55], v112
	v_smfmac_f32_16x16x64_f16 v[144:147], v[120:123], v[72:79], v112
	s_waitcnt lgkmcnt(0)
	v_smfmac_f32_16x16x64_f16 v[136:139], v[124:127], v[32:39], v112
	v_smfmac_f32_16x16x64_f16 v[148:151], v[124:127], v[104:111], v112
	v_smfmac_f32_16x16x64_f16 v[140:143], v[124:127], v[56:63], v112
	v_smfmac_f32_16x16x64_f16 v[144:147], v[124:127], v[80:87], v112
	s_nop 8
	v_add_f32_e32 v153, v136, v137
	v_add_f32_e32 v156, v148, v149
	v_add_f32_e32 v154, v140, v141
	v_add_f32_e32 v155, v144, v145
	v_mov_b32_dpp v157, v156 row_shl:3 row_mask:0xf bank_mask:0xf bound_ctrl:1
	v_mov_b32_dpp v158, v156 row_shl:6 row_mask:0xf bank_mask:0xf bound_ctrl:1
	v_cndmask_b32_e64 v159, v156, v153, s[28:29]
	v_exp_f32_e32 v159, v159
	v_cndmask_b32_e64 v160, v157, v154, s[28:29]
	v_exp_f32_e32 v160, v160
	v_cndmask_b32_e64 v155, v158, v155, s[28:29]
	v_add_f32_e32 v159, 1.0, v159
	v_rcp_f32_e32 v159, v159
	v_add_f32_e32 v160, 1.0, v160
	v_rcp_f32_e32 v160, v160
	v_fmac_f32_e32 v152, v159, v155
	v_exp_f32_e32 v152, v152
	ds_read_b32 v136, v163 offset:24960
	ds_read_b32 v140, v164 offset:24960
	ds_read_b32 v148, v165 offset:24960
	v_mov_b32_e32 v144, v113
	v_mov_b32_e32 v137, 0
	v_mov_b32_e32 v141, 0
	v_mov_b32_e32 v145, 0
	v_mov_b32_e32 v149, 0
	v_add_f32_e32 v152, 1.0, v152
	v_rcp_f32_e32 v159, v152
	s_nop 0
	v_fma_f32 v159, v159, -2.0, 1.0
	ds_read_b32 v152, v166 offset:24960
	v_sub_f32_e32 v153, v161, v159
	v_fma_mixlo_f16 v162, v160, v153, v159
	v_fma_f32 v161, v160, v153, v159
	ds_write_b16 v168, v162 offset:384
	global_store_dword v[170:171], v161, off
	v_lshl_add_u64 v[170:171], v[170:171], 0, s[20:21]
	s_waitcnt lgkmcnt(0)
	s_barrier
	ds_read_b128 v[116:119], v167 offset:384
	ds_read_b128 v[120:123], v167 offset:512
	ds_read_b128 v[124:127], v167 offset:640
	s_waitcnt lgkmcnt(2)
	v_smfmac_f32_16x16x64_f16 v[136:139], v[116:119], v[16:23], v112
	v_smfmac_f32_16x16x64_f16 v[148:151], v[116:119], v[88:95], v112
	v_smfmac_f32_16x16x64_f16 v[140:143], v[116:119], v[40:47], v112
	v_smfmac_f32_16x16x64_f16 v[144:147], v[116:119], v[64:71], v112
	s_waitcnt lgkmcnt(1)
	v_smfmac_f32_16x16x64_f16 v[136:139], v[120:123], v[24:31], v112
	v_smfmac_f32_16x16x64_f16 v[148:151], v[120:123], v[96:103], v112
	v_smfmac_f32_16x16x64_f16 v[140:143], v[120:123], v[48:55], v112
	v_smfmac_f32_16x16x64_f16 v[144:147], v[120:123], v[72:79], v112
	s_waitcnt lgkmcnt(0)
	v_smfmac_f32_16x16x64_f16 v[136:139], v[124:127], v[32:39], v112
	v_smfmac_f32_16x16x64_f16 v[148:151], v[124:127], v[104:111], v112
	v_smfmac_f32_16x16x64_f16 v[140:143], v[124:127], v[56:63], v112
	v_smfmac_f32_16x16x64_f16 v[144:147], v[124:127], v[80:87], v112
	s_nop 8
	v_add_f32_e32 v153, v136, v137
	v_add_f32_e32 v156, v148, v149
	v_add_f32_e32 v154, v140, v141
	v_add_f32_e32 v155, v144, v145
	v_mov_b32_dpp v157, v156 row_shl:3 row_mask:0xf bank_mask:0xf bound_ctrl:1
	v_mov_b32_dpp v158, v156 row_shl:6 row_mask:0xf bank_mask:0xf bound_ctrl:1
	v_cndmask_b32_e64 v159, v156, v153, s[28:29]
	v_exp_f32_e32 v159, v159
	v_cndmask_b32_e64 v160, v157, v154, s[28:29]
	v_exp_f32_e32 v160, v160
	v_cndmask_b32_e64 v155, v158, v155, s[28:29]
	v_add_f32_e32 v159, 1.0, v159
	v_rcp_f32_e32 v159, v159
	v_add_f32_e32 v160, 1.0, v160
	v_rcp_f32_e32 v160, v160
	v_fmac_f32_e32 v152, v159, v155
	v_exp_f32_e32 v152, v152
	ds_read_b32 v136, v163 offset:26880
	ds_read_b32 v140, v164 offset:26880
	ds_read_b32 v148, v165 offset:26880
	v_mov_b32_e32 v144, v113
	v_mov_b32_e32 v137, 0
	v_mov_b32_e32 v141, 0
	v_mov_b32_e32 v145, 0
	v_mov_b32_e32 v149, 0
	v_add_f32_e32 v152, 1.0, v152
	v_rcp_f32_e32 v159, v152
	s_nop 0
	v_fma_f32 v159, v159, -2.0, 1.0
	ds_read_b32 v152, v166 offset:26880
	v_sub_f32_e32 v153, v161, v159
	v_fma_mixlo_f16 v162, v160, v153, v159
	v_fma_f32 v161, v160, v153, v159
	ds_write_b16 v168, v162 offset:0
	global_store_dword v[170:171], v161, off
	v_lshl_add_u64 v[170:171], v[170:171], 0, s[20:21]
	s_waitcnt lgkmcnt(0)
	s_barrier
	ds_read_b128 v[116:119], v167 offset:0
	ds_read_b128 v[120:123], v167 offset:128
	ds_read_b128 v[124:127], v167 offset:256
	s_waitcnt lgkmcnt(2)
	v_smfmac_f32_16x16x64_f16 v[136:139], v[116:119], v[16:23], v112
	v_smfmac_f32_16x16x64_f16 v[148:151], v[116:119], v[88:95], v112
	v_smfmac_f32_16x16x64_f16 v[140:143], v[116:119], v[40:47], v112
	v_smfmac_f32_16x16x64_f16 v[144:147], v[116:119], v[64:71], v112
	s_waitcnt lgkmcnt(1)
	v_smfmac_f32_16x16x64_f16 v[136:139], v[120:123], v[24:31], v112
	v_smfmac_f32_16x16x64_f16 v[148:151], v[120:123], v[96:103], v112
	v_smfmac_f32_16x16x64_f16 v[140:143], v[120:123], v[48:55], v112
	v_smfmac_f32_16x16x64_f16 v[144:147], v[120:123], v[72:79], v112
	s_waitcnt lgkmcnt(0)
	v_smfmac_f32_16x16x64_f16 v[136:139], v[124:127], v[32:39], v112
	v_smfmac_f32_16x16x64_f16 v[148:151], v[124:127], v[104:111], v112
	v_smfmac_f32_16x16x64_f16 v[140:143], v[124:127], v[56:63], v112
	v_smfmac_f32_16x16x64_f16 v[144:147], v[124:127], v[80:87], v112
	s_nop 8
	v_add_f32_e32 v153, v136, v137
	v_add_f32_e32 v156, v148, v149
	v_add_f32_e32 v154, v140, v141
	v_add_f32_e32 v155, v144, v145
	v_mov_b32_dpp v157, v156 row_shl:3 row_mask:0xf bank_mask:0xf bound_ctrl:1
	v_mov_b32_dpp v158, v156 row_shl:6 row_mask:0xf bank_mask:0xf bound_ctrl:1
	v_cndmask_b32_e64 v159, v156, v153, s[28:29]
	v_exp_f32_e32 v159, v159
	v_cndmask_b32_e64 v160, v157, v154, s[28:29]
	v_exp_f32_e32 v160, v160
	v_cndmask_b32_e64 v155, v158, v155, s[28:29]
	v_add_f32_e32 v159, 1.0, v159
	v_rcp_f32_e32 v159, v159
	v_add_f32_e32 v160, 1.0, v160
	v_rcp_f32_e32 v160, v160
	v_fmac_f32_e32 v152, v159, v155
	v_exp_f32_e32 v152, v152
	ds_read_b32 v136, v163 offset:28800
	ds_read_b32 v140, v164 offset:28800
	ds_read_b32 v148, v165 offset:28800
	v_mov_b32_e32 v144, v113
	v_mov_b32_e32 v137, 0
	v_mov_b32_e32 v141, 0
	v_mov_b32_e32 v145, 0
	v_mov_b32_e32 v149, 0
	v_add_f32_e32 v152, 1.0, v152
	v_rcp_f32_e32 v159, v152
	s_nop 0
	v_fma_f32 v159, v159, -2.0, 1.0
	ds_read_b32 v152, v166 offset:28800
	v_sub_f32_e32 v153, v161, v159
	v_fma_mixlo_f16 v162, v160, v153, v159
	v_fma_f32 v161, v160, v153, v159
	ds_write_b16 v168, v162 offset:384
	global_store_dword v[170:171], v161, off
	v_lshl_add_u64 v[170:171], v[170:171], 0, s[20:21]
	s_waitcnt lgkmcnt(0)
	s_barrier
	ds_read_b128 v[116:119], v167 offset:384
	ds_read_b128 v[120:123], v167 offset:512
	ds_read_b128 v[124:127], v167 offset:640
	s_waitcnt lgkmcnt(2)
	v_smfmac_f32_16x16x64_f16 v[136:139], v[116:119], v[16:23], v112
	v_smfmac_f32_16x16x64_f16 v[148:151], v[116:119], v[88:95], v112
	v_smfmac_f32_16x16x64_f16 v[140:143], v[116:119], v[40:47], v112
	v_smfmac_f32_16x16x64_f16 v[144:147], v[116:119], v[64:71], v112
	s_waitcnt lgkmcnt(1)
	v_smfmac_f32_16x16x64_f16 v[136:139], v[120:123], v[24:31], v112
	v_smfmac_f32_16x16x64_f16 v[148:151], v[120:123], v[96:103], v112
	v_smfmac_f32_16x16x64_f16 v[140:143], v[120:123], v[48:55], v112
	v_smfmac_f32_16x16x64_f16 v[144:147], v[120:123], v[72:79], v112
	s_waitcnt lgkmcnt(0)
	v_smfmac_f32_16x16x64_f16 v[136:139], v[124:127], v[32:39], v112
	v_smfmac_f32_16x16x64_f16 v[148:151], v[124:127], v[104:111], v112
	v_smfmac_f32_16x16x64_f16 v[140:143], v[124:127], v[56:63], v112
	v_smfmac_f32_16x16x64_f16 v[144:147], v[124:127], v[80:87], v112
	s_nop 8
	v_add_f32_e32 v153, v136, v137
	v_add_f32_e32 v156, v148, v149
	v_add_f32_e32 v154, v140, v141
	v_add_f32_e32 v155, v144, v145
	v_mov_b32_dpp v157, v156 row_shl:3 row_mask:0xf bank_mask:0xf bound_ctrl:1
	v_mov_b32_dpp v158, v156 row_shl:6 row_mask:0xf bank_mask:0xf bound_ctrl:1
	v_cndmask_b32_e64 v159, v156, v153, s[28:29]
	v_exp_f32_e32 v159, v159
	v_cndmask_b32_e64 v160, v157, v154, s[28:29]
	v_exp_f32_e32 v160, v160
	v_cndmask_b32_e64 v155, v158, v155, s[28:29]
	v_add_f32_e32 v159, 1.0, v159
	v_rcp_f32_e32 v159, v159
	v_add_f32_e32 v160, 1.0, v160
	v_rcp_f32_e32 v160, v160
	v_xor_b32_e32 v163, 0x7800, v163
	v_xor_b32_e32 v164, 0x7800, v164
	v_xor_b32_e32 v165, 0x7800, v165
	v_xor_b32_e32 v166, 0x7800, v166
	v_add_u32_e32 v173, s55, v173
	v_add_u32_e32 v174, s55, v174
	v_add_u32_e32 v115, s55, v115
	v_add_u32_e32 v169, s55, v169
	s_sub_i32 s55, 0, s55
	v_fmac_f32_e32 v152, v159, v155
	v_exp_f32_e32 v152, v152
	ds_read_b32 v136, v163 offset:0
	ds_read_b32 v140, v164 offset:0
	ds_read_b32 v148, v165 offset:0
	v_mov_b32_e32 v144, v113
	v_mov_b32_e32 v137, 0
	v_mov_b32_e32 v141, 0
	v_mov_b32_e32 v145, 0
	v_mov_b32_e32 v149, 0
	v_add_f32_e32 v152, 1.0, v152
	v_rcp_f32_e32 v159, v152
	s_nop 0
	v_fma_f32 v159, v159, -2.0, 1.0
	ds_read_b32 v152, v166 offset:0
	v_sub_f32_e32 v153, v161, v159
	v_fma_mixlo_f16 v162, v160, v153, v159
	v_fma_f32 v161, v160, v153, v159
	ds_write_b16 v168, v162 offset:0
	global_store_dword v[170:171], v161, off
	v_lshl_add_u64 v[170:171], v[170:171], 0, s[20:21]
	s_waitcnt lgkmcnt(0)
	s_barrier
	s_add_i32 s26, s26, 1
	s_cmp_lt_u32 s26, 8
	s_cbranch_scc1 .Lgru1_chunk
.LBB5_143:
	s_endpgm
	s_nop 0
	s_endpgm

	.amdhsa_kernel _Z15gru_mfma_kernelILi1EEvPKfmS1_S1_S1_S1_PfS2_i7PreArgs
		.amdhsa_group_segment_fixed_size 62720
		.amdhsa_private_segment_fixed_size 0
		.amdhsa_kernarg_size 448
		.amdhsa_user_sgpr_count 2
		.amdhsa_user_sgpr_dispatch_ptr 0
		.amdhsa_user_sgpr_queue_ptr 0
		.amdhsa_user_sgpr_kernarg_segment_ptr 1
		.amdhsa_user_sgpr_dispatch_id 0
		.amdhsa_user_sgpr_kernarg_preload_length 0
		.amdhsa_user_sgpr_kernarg_preload_offset 0
		.amdhsa_user_sgpr_private_segment_size 0
		.amdhsa_uses_dynamic_stack 0
		.amdhsa_enable_private_segment 0
		.amdhsa_system_sgpr_workgroup_id_x 1
		.amdhsa_system_sgpr_workgroup_id_y 0
		.amdhsa_system_sgpr_workgroup_id_z 0
		.amdhsa_system_sgpr_workgroup_info 0
		.amdhsa_system_vgpr_workitem_id 0
		.amdhsa_next_free_vgpr 192
		.amdhsa_next_free_sgpr 96
		.amdhsa_accum_offset 192
		.amdhsa_reserve_vcc 1
		.amdhsa_float_round_mode_32 0
		.amdhsa_float_round_mode_16_64 0
		.amdhsa_float_denorm_mode_32 3
		.amdhsa_float_denorm_mode_16_64 3
		.amdhsa_dx10_clamp 1
		.amdhsa_ieee_mode 1
		.amdhsa_fp16_overflow 0
		.amdhsa_tg_split 0
		.amdhsa_exception_fp_ieee_invalid_op 0
		.amdhsa_exception_fp_denorm_src 0
		.amdhsa_exception_fp_ieee_div_zero 0
		.amdhsa_exception_fp_ieee_overflow 0
		.amdhsa_exception_fp_ieee_underflow 0
		.amdhsa_exception_fp_ieee_inexact 0
		.amdhsa_exception_int_div_zero 0
	.end_amdhsa_kernel

.LBB6_26:
	s_and_b64 vcc, exec, s[4:5]
	s_cbranch_vccz .LBB6_81
	s_setprio 3
	s_load_dwordx2 s[8:9], s[0:1], 0x0
	s_load_dwordx2 s[10:11], s[0:1], 0x8
	s_load_dwordx2 s[12:13], s[0:1], 0x18
	s_load_dwordx2 s[32:33], s[0:1], 0x28
	s_load_dwordx4 s[36:39], s[0:1], 0x30
	s_load_dwordx2 s[18:19], s[0:1], 0xb8
	s_load_dwordx2 s[16:17], s[0:1], 0xc8
	s_load_dword s34, s[0:1], 0xd4
	s_lshr_b32 s3, s2, 4
	s_bfe_u32 s4, s2, 0x10003
	s_and_b32 s5, s2, 7
	v_lshrrev_b32_e32 v1, 6, v0
	v_and_b32_e32 v2, 63, v0
	v_and_b32_e32 v3, 15, v0
	v_bfe_u32 v4, v0, 4, 2
	s_nop 1
	v_readfirstlane_b32 s6, v1
	s_waitcnt lgkmcnt(0)
	s_cmp_eq_u32 s3, 0
	s_cselect_b32 s12, s12, s32
	s_cselect_b32 s13, s13, s33
	s_cselect_b32 s14, s36, s38
	s_cselect_b32 s15, s37, s39
	s_mul_i32 s35, s4, 0x708
	s_add_u32 s12, s12, s35
	s_addc_u32 s13, s13, 0
	s_mul_i32 s35, s5, 0x25800
	s_add_u32 s14, s14, s35
	s_addc_u32 s15, s15, 0
	s_mul_i32 s35, s4, 0x258
	s_add_u32 s14, s14, s35
	s_addc_u32 s15, s15, 0
	s_lshl_b64 s[10:11], s[10:11], 2
	s_mul_i32 s35, s3, 0x384000
	s_add_u32 s8, s8, s35
	s_addc_u32 s9, s9, 0
	s_mul_i32 s35, s5, 0x70800
	s_add_u32 s8, s8, s35
	s_addc_u32 s9, s9, 0
	s_mul_i32 s35, s4, 0x708
	s_add_u32 s8, s8, s35
	s_addc_u32 s9, s9, 0
	s_mul_i32 s35, s4, 112
	s_lshl_b32 s40, s6, 1
	s_add_i32 s35, s35, s40
	s_mul_i32 s35, s35, 0xe10
	s_add_u32 s22, s8, s35
	s_addc_u32 s23, s9, 0
	s_add_u32 s46, s22, 0xe10
	s_addc_u32 s47, s23, 0
	s_add_u32 s24, s22, s10
	s_addc_u32 s25, s23, s11
	s_add_u32 s48, s24, 0xe10
	s_addc_u32 s49, s25, 0
	s_cmp_eq_u32 s4, 0
	s_mov_b32 s27, 0xffff1f00
	s_mov_b32 s20, 0xfffffb50
	s_cselect_b32 s27, 0xe100, s27
	s_cselect_b32 s50, 0, -1
	s_cselect_b32 s20, 0x4b0, s20
	s_cselect_b32 s21, 0, -1
	s_lshl_b32 s35, s3, 1
	s_add_i32 s35, s35, s4
	s_add_i32 s35, s35, s34
	s_mul_i32 s35, s35, 0x28000
	s_add_u32 s16, s16, s35
	s_addc_u32 s17, s17, 0
	s_mul_i32 s35, s6, 0x5000
	s_add_u32 s16, s16, s35
	s_addc_u32 s17, s17, 0
	s_mov_b32 s28, 0xffff
	s_mov_b32 s29, 0
	s_mov_b32 s30, -1
	s_mov_b32 s31, 1
	s_mov_b32 s51, 0xbfb8aa3b
	s_mov_b32 s52, 0x4038aa3b
	v_lshlrev_b32_e32 v5, 4, v2
	v_mov_b32_e32 v36, 0
	v_mov_b32_e32 v37, 0
	v_mov_b32_e32 v38, 0
	v_mov_b32_e32 v39, 0
	v_mov_b32_e32 v60, 0
	v_mov_b32_e32 v61, 0
	v_mov_b32_e32 v62, 0
	v_mov_b32_e32 v63, 0
	v_mov_b32_e32 v84, 0
	v_mov_b32_e32 v85, 0
	v_mov_b32_e32 v86, 0
	v_mov_b32_e32 v87, 0
	v_mov_b32_e32 v108, 0
	v_mov_b32_e32 v109, 0
	v_mov_b32_e32 v110, 0
	v_mov_b32_e32 v111, 0
	s_add_u32 s42, s16, 0x0
	s_addc_u32 s43, s17, 0
	global_load_dwordx4 v[16:19], v5, s[42:43] offset:0
	global_load_dwordx4 v[20:23], v5, s[42:43] offset:1024
	global_load_dwordx4 v[24:27], v5, s[42:43] offset:2048
	global_load_dwordx4 v[28:31], v5, s[42:43] offset:3072
	s_add_u32 s42, s16, 0x1000
	s_addc_u32 s43, s17, 0
	global_load_dwordx4 v[32:35], v5, s[42:43]
	s_add_u32 s42, s16, 0x1400
	s_addc_u32 s43, s17, 0
	global_load_dwordx4 v[40:43], v5, s[42:43] offset:0
	global_load_dwordx4 v[44:47], v5, s[42:43] offset:1024
	global_load_dwordx4 v[48:51], v5, s[42:43] offset:2048
	global_load_dwordx4 v[52:55], v5, s[42:43] offset:3072
	s_add_u32 s42, s16, 0x2400
	s_addc_u32 s43, s17, 0
	global_load_dwordx4 v[56:59], v5, s[42:43]
	s_add_u32 s42, s16, 0x2800
	s_addc_u32 s43, s17, 0
	global_load_dwordx4 v[64:67], v5, s[42:43] offset:0
	global_load_dwordx4 v[68:71], v5, s[42:43] offset:1024
	global_load_dwordx4 v[72:75], v5, s[42:43] offset:2048
	global_load_dwordx4 v[76:79], v5, s[42:43] offset:3072
	s_add_u32 s42, s16, 0x3800
	s_addc_u32 s43, s17, 0
	global_load_dwordx4 v[80:83], v5, s[42:43]
	s_add_u32 s42, s16, 0x3c00
	s_addc_u32 s43, s17, 0
	global_load_dwordx4 v[88:91], v5, s[42:43] offset:0
	global_load_dwordx4 v[92:95], v5, s[42:43] offset:1024
	global_load_dwordx4 v[96:99], v5, s[42:43] offset:2048
	global_load_dwordx4 v[100:103], v5, s[42:43] offset:3072
	s_add_u32 s42, s16, 0x4c00
	s_addc_u32 s43, s17, 0
	global_load_dwordx4 v[104:107], v5, s[42:43]
	v_and_b32_e32 v6, 1, v3
	v_cmp_eq_u32_e32 vcc, 1, v6
	v_mov_b32_e32 v7, 0x44444444
	v_mov_b32_e32 v8, 0xeeeeeeee
	s_nop 1
	v_cndmask_b32_e32 v112, v7, v8, vcc
	s_mul_i32 s53, s6, 19
	v_add_u32_e32 v6, s53, v3
	v_cmp_gt_u32_e32 vcc, 0x96, v6
	v_add_u32_e32 v7, 0x12c, v6
	v_mov_b32_e32 v8, 0x12c
	s_nop 1
	v_cndmask_b32_e32 v7, v8, v7, vcc
	v_lshlrev_b32_e32 v7, 2, v7
	global_load_dword v9, v7, s[12:13]
	s_mov_b64 s[54:55], vcc
	v_cmp_gt_u32_e32 vcc, 0xc0, v0
	v_lshlrev_b32_e32 v10, 2, v0
	v_mov_b32_e32 v11, 0
	s_and_saveexec_b64 s[44:45], vcc
	ds_write_b32 v10, v11 offset:61440
	s_mov_b64 exec, s[44:45]
	v_and_b32_e32 v10, 31, v0
	v_lshrrev_b32_e32 v11, 5, v0
	v_subrev_u32_e32 v12, 6, v10
	v_max_i32_e32 v12, 0, v12
	v_mul_u32_u24_e32 v13, 11, v12
	v_lshrrev_b32_e32 v13, 5, v13
	v_mul_u32_u24_e32 v14, 3, v13
	v_sub_u32_e32 v14, v12, v14
	v_mul_u32_u24_e32 v15, 19, v13
	v_add3_u32 v15, v15, v14, 16
	v_cmp_gt_u32_e32 vcc, 0x96, v15
	v_cmp_lt_u32_e64 s[56:57], 5, v10
	v_cmp_gt_u32_e64 s[58:59], 30, v10
	s_and_b64 s[56:57], s[56:57], vcc
	s_and_b64 s[56:57], s[56:57], s[58:59]
	v_add_u32_e32 v15, 0x12c, v15
	v_mov_b32_e32 v14, 0x12c
	v_cndmask_b32_e64 v15, v14, v15, s[56:57]
	v_lshlrev_b32_e32 v15, 2, v15
	global_load_dword v14, v15, s[12:13]
	v_mul_u32_u24_e32 v11, 0x780, v11
	v_lshl_add_u32 v11, v10, 2, v11
	s_waitcnt vmcnt(0)
	v_mul_f32_e32 v14, s52, v14
	v_mul_f32_e32 v9, s52, v9
	v_cndmask_b32_e64 v14, 0, v14, s[56:57]
	v_cndmask_b32_e64 v113, 0, v9, s[54:55]
	s_and_saveexec_b64 s[44:45], s[58:59]
	ds_write_b32 v11, v14 offset:1800
	ds_write_b32 v11, v14 offset:32520
	s_mov_b64 exec, s[44:45]
	v_lshlrev_b32_e32 v172, 3, v2
	s_lshl_b32 s35, s6, 1
	s_sub_i32 s40, 15, s35
	s_cmp_eq_u32 s4, 0
	s_cselect_b32 s41, s35, s40
	s_add_i32 s35, s35, 1
	s_sub_i32 s40, 15, s35
	s_cmp_eq_u32 s4, 0
	s_cselect_b32 s40, s35, s40
	s_mul_i32 s41, s41, 0x780
	s_mul_i32 s40, s40, 0x780
	v_add_u32_e32 v173, s41, v172
	v_add_u32_e32 v174, s40, v172
	v_min_u32_e32 v6, 32, v2
	v_lshlrev_b32_e32 v114, 3, v6
	v_add_u32_e32 v115, s41, v114
	v_add_u32_e32 v169, s40, v114
	v_cmp_lt_u32_e32 vcc, 21, v2
	v_mov_b32_e32 v6, s51
	v_mov_b32_e32 v7, s52
	s_nop 0
	v_cndmask_b32_e32 v175, v6, v7, vcc
	global_load_dwordx2 v[176:177], v172, s[22:23] offset:0
	global_load_dwordx2 v[178:179], v172, s[22:23] offset:512
	global_load_dwordx2 v[180:181], v172, s[22:23] offset:1024
	global_load_dwordx2 v[192:193], v172, s[24:25] offset:0
	global_load_dwordx2 v[194:195], v172, s[24:25] offset:512
	global_load_dwordx2 v[196:197], v172, s[24:25] offset:1024
	global_load_dwordx2 v[184:185], v172, s[46:47] offset:0
	global_load_dwordx2 v[186:187], v172, s[46:47] offset:512
	global_load_dwordx2 v[188:189], v172, s[46:47] offset:1024
	global_load_dwordx2 v[200:201], v172, s[48:49] offset:0
	global_load_dwordx2 v[202:203], v172, s[48:49] offset:512
	global_load_dwordx2 v[204:205], v172, s[48:49] offset:1024
	global_load_dwordx2 v[182:183], v114, s[22:23] offset:1536
	global_load_dwordx2 v[198:199], v114, s[24:25] offset:1536
	global_load_dwordx2 v[190:191], v114, s[46:47] offset:1536
	global_load_dwordx2 v[206:207], v114, s[48:49] offset:1536
	s_waitcnt vmcnt(0)
	v_add_f32_e32 v176, v176, v192
	v_add_f32_e32 v177, v177, v193
	v_mul_f32_e32 v176, s51, v176
	v_mul_f32_e32 v177, s51, v177
	v_add_f32_e32 v178, v178, v194
	v_add_f32_e32 v179, v179, v195
	v_mul_f32_e32 v178, s51, v178
	v_mul_f32_e32 v179, s51, v179
	v_add_f32_e32 v180, v180, v196
	v_add_f32_e32 v181, v181, v197
	v_mul_f32_e32 v180, v175, v180
	v_mul_f32_e32 v181, v175, v181
	v_add_f32_e32 v182, v182, v198
	v_add_f32_e32 v183, v183, v199
	v_mul_f32_e32 v182, s52, v182
	v_mul_f32_e32 v183, s52, v183
	ds_write_b64 v173, v[176:177] offset:0
	ds_write_b64 v173, v[178:179] offset:512
	ds_write_b64 v173, v[180:181] offset:1024
	ds_write_b64 v115, v[182:183] offset:1536
	v_add_f32_e32 v184, v184, v200
	v_add_f32_e32 v185, v185, v201
	v_mul_f32_e32 v184, s51, v184
	v_mul_f32_e32 v185, s51, v185
	v_add_f32_e32 v186, v186, v202
	v_add_f32_e32 v187, v187, v203
	v_mul_f32_e32 v186, s51, v186
	v_mul_f32_e32 v187, s51, v187
	v_add_f32_e32 v188, v188, v204
	v_add_f32_e32 v189, v189, v205
	v_mul_f32_e32 v188, v175, v188
	v_mul_f32_e32 v189, v175, v189
	v_add_f32_e32 v190, v190, v206
	v_add_f32_e32 v191, v191, v207
	v_mul_f32_e32 v190, s52, v190
	v_mul_f32_e32 v191, s52, v191
	ds_write_b64 v174, v[184:185] offset:0
	ds_write_b64 v174, v[186:187] offset:512
	ds_write_b64 v174, v[188:189] offset:1024
	ds_write_b64 v169, v[190:191] offset:1536
	s_movk_i32 s55, 0x7800
	v_add_u32_e32 v173, s55, v173
	v_add_u32_e32 v174, s55, v174
	v_add_u32_e32 v115, s55, v115
	v_add_u32_e32 v169, s55, v169
	s_sub_i32 s55, 0, s55
	v_add_u32_e32 v6, s53, v2
	v_cmp_gt_u32_e32 vcc, 0x96, v6
	v_cmp_gt_u32_e64 s[56:57], 16, v2
	v_cmp_gt_u32_e64 s[58:59], 19, v2
	s_and_b64 s[56:57], s[56:57], vcc
	s_and_b64 s[58:59], s[58:59], vcc
	v_mov_b32_e32 v7, 0x710
	v_lshlrev_b32_e32 v8, 2, v6
	v_add_u32_e32 v9, 0x258, v8
	v_add_u32_e32 v10, 0x4b0, v8
	v_cndmask_b32_e64 v163, v7, v8, s[56:57]
	v_cndmask_b32_e64 v164, v7, v9, s[56:57]
	v_cndmask_b32_e64 v166, v7, v10, s[58:59]
	v_subrev_u32_e32 v9, 16, v2
	v_cmp_gt_u32_e64 s[60:61], 6, v9
	v_cmp_lt_u32_e32 vcc, 2, v9
	v_mov_b32_e32 v11, 0x93
	s_nop 0
	v_cndmask_b32_e32 v10, 0, v11, vcc
	v_cndmask_b32_e64 v12, 0, 3, vcc
	v_sub_u32_e32 v13, v6, v12
	v_cmp_gt_u32_e32 vcc, 0x96, v13
	s_and_b64 s[60:61], s[60:61], vcc
	v_add_u32_e32 v13, v6, v10
	v_lshlrev_b32_e32 v13, 2, v13
	v_cndmask_b32_e64 v165, v7, v13, s[60:61]
	v_subrev_u32_e32 v9, 22, v2
	v_cmp_gt_u32_e32 vcc, 3, v9
	s_mul_i32 s35, s6, 3
	s_addk_i32 s35, 0x1c8
	v_add_lshl_u32 v9, v9, s35, 2
	s_nop 0
	v_cndmask_b32_e32 v165, v165, v9, vcc
	v_and_b32_e32 v9, 1, v3
	v_lshlrev_b32_e32 v9, 4, v9
	v_lshl_or_b32 v9, v4, 5, v9
	v_add_u32_e32 v167, 0xf000, v9
	v_and_b32_e32 v9, 0xfffffff0, v6
	v_bfe_u32 v10, v6, 1, 1
	v_lshl_or_b32 v9, v10, 3, v9
	v_bfe_u32 v10, v6, 2, 2
	v_lshl_or_b32 v9, v10, 1, v9
	v_and_b32_e32 v10, 1, v6
	v_or_b32_e32 v9, v9, v10
	v_lshlrev_b32_e32 v9, 1, v9
	v_add_u32_e32 v9, 0xf000, v9
	v_lshlrev_b32_e32 v10, 1, v2
	v_add_u32_e32 v10, 0xf300, v10
	v_cndmask_b32_e64 v168, v10, v9, s[58:59]
	s_mul_i32 s35, s4, 0x25350
	s_add_u32 s14, s14, s35
	s_addc_u32 s15, s15, 0
	s_add_u32 s18, s18, 0x25800
	s_addc_u32 s19, s19, 0
	v_lshlrev_b32_e32 v9, 2, v0
	v_mov_b32_e32 v10, s18
	v_mov_b32_e32 v11, s19
	v_mov_b32_e32 v12, s14
	v_mov_b32_e32 v13, s15
	v_cndmask_b32_e64 v9, v9, v8, s[58:59]
	v_cndmask_b32_e64 v10, v10, v12, s[58:59]
	v_cndmask_b32_e64 v11, v11, v13, s[58:59]
	v_add_co_u32_e32 v170, vcc, v10, v9
	s_nop 1
	v_addc_co_u32_e32 v171, vcc, 0, v11, vcc
	v_mov_b32_e32 v161, 0
	v_mov_b32_e32 v137, 0
	v_mov_b32_e32 v138, 0
	v_mov_b32_e32 v139, 0
	v_mov_b32_e32 v141, 0
	v_mov_b32_e32 v142, 0
	v_mov_b32_e32 v143, 0
	v_mov_b32_e32 v145, 0
	v_mov_b32_e32 v146, 0
	v_mov_b32_e32 v147, 0
	v_mov_b32_e32 v149, 0
	v_mov_b32_e32 v150, 0
	v_mov_b32_e32 v151, 0
	s_mov_b32 s26, 0
	s_waitcnt vmcnt(0) lgkmcnt(0)
	s_barrier
	ds_read_b32 v136, v163 offset:0
	ds_read_b32 v140, v164 offset:0
	ds_read_b32 v148, v165 offset:0
	ds_read_b32 v152, v166 offset:0
	v_mov_b32_e32 v144, v113
	s_waitcnt lgkmcnt(0)
.Lgru2_chunk:
	ds_read_b128 v[116:119], v167 offset:0
	ds_read_b128 v[120:123], v167 offset:128
	ds_read_b128 v[124:127], v167 offset:256
	s_waitcnt lgkmcnt(2)
	v_smfmac_f32_16x16x64_f16 v[136:139], v[116:119], v[16:23], v112
	v_smfmac_f32_16x16x64_f16 v[148:151], v[116:119], v[88:95], v112
	v_smfmac_f32_16x16x64_f16 v[140:143], v[116:119], v[40:47], v112
	v_smfmac_f32_16x16x64_f16 v[144:147], v[116:119], v[64:71], v112
	s_waitcnt lgkmcnt(1)
	v_smfmac_f32_16x16x64_f16 v[136:139], v[120:123], v[24:31], v112
	v_smfmac_f32_16x16x64_f16 v[148:151], v[120:123], v[96:103], v112
	v_smfmac_f32_16x16x64_f16 v[140:143], v[120:123], v[48:55], v112
	v_smfmac_f32_16x16x64_f16 v[144:147], v[120:123], v[72:79], v112
	s_waitcnt lgkmcnt(0)
	v_smfmac_f32_16x16x64_f16 v[136:139], v[124:127], v[32:39], v112
	v_smfmac_f32_16x16x64_f16 v[148:151], v[124:127], v[104:111], v112
	v_smfmac_f32_16x16x64_f16 v[140:143], v[124:127], v[56:63], v112
	v_smfmac_f32_16x16x64_f16 v[144:147], v[124:127], v[80:87], v112
	s_nop 8
	v_add_f32_e32 v153, v136, v137
	v_add_f32_e32 v156, v148, v149
	v_add_f32_e32 v154, v140, v141
	v_add_f32_e32 v155, v144, v145
	v_mov_b32_dpp v157, v156 row_shl:3 row_mask:0xf bank_mask:0xf bound_ctrl:1
	v_mov_b32_dpp v158, v156 row_shl:6 row_mask:0xf bank_mask:0xf bound_ctrl:1
	v_cndmask_b32_e64 v159, v156, v153, s[28:29]
	v_exp_f32_e32 v159, v159
	v_cndmask_b32_e64 v160, v157, v154, s[28:29]
	v_exp_f32_e32 v160, v160
	v_cndmask_b32_e64 v155, v158, v155, s[28:29]
	v_add_f32_e32 v159, 1.0, v159
	v_rcp_f32_e32 v159, v159
	v_add_f32_e32 v160, 1.0, v160
	v_rcp_f32_e32 v160, v160
	v_fmac_f32_e32 v152, v159, v155
	v_exp_f32_e32 v152, v152
	ds_read_b32 v136, v163 offset:1920
	ds_read_b32 v140, v164 offset:1920
	ds_read_b32 v148, v165 offset:1920
	v_mov_b32_e32 v144, v113
	v_mov_b32_e32 v137, 0
	v_mov_b32_e32 v141, 0
	v_mov_b32_e32 v145, 0
	v_mov_b32_e32 v149, 0
	v_add_f32_e32 v152, 1.0, v152
	v_rcp_f32_e32 v159, v152
	s_nop 0
	v_fma_f32 v159, v159, -2.0, 1.0
	ds_read_b32 v152, v166 offset:1920
	v_sub_f32_e32 v153, v161, v159
	v_fma_mixlo_f16 v162, v160, v153, v159
	v_fma_f32 v161, v160, v153, v159
	ds_write_b16 v168, v162 offset:384
	global_store_dword v[170:171], v161, off
	v_lshl_add_u64 v[170:171], v[170:171], 0, s[20:21]
	s_waitcnt lgkmcnt(0)
	s_barrier
	ds_read_b128 v[116:119], v167 offset:384
	ds_read_b128 v[120:123], v167 offset:512
	ds_read_b128 v[124:127], v167 offset:640
	s_waitcnt lgkmcnt(2)
	v_smfmac_f32_16x16x64_f16 v[136:139], v[116:119], v[16:23], v112
	v_smfmac_f32_16x16x64_f16 v[148:151], v[116:119], v[88:95], v112
	v_smfmac_f32_16x16x64_f16 v[140:143], v[116:119], v[40:47], v112
	v_smfmac_f32_16x16x64_f16 v[144:147], v[116:119], v[64:71], v112
	s_waitcnt lgkmcnt(1)
	v_smfmac_f32_16x16x64_f16 v[136:139], v[120:123], v[24:31], v112
	v_smfmac_f32_16x16x64_f16 v[148:151], v[120:123], v[96:103], v112
	v_smfmac_f32_16x16x64_f16 v[140:143], v[120:123], v[48:55], v112
	v_smfmac_f32_16x16x64_f16 v[144:147], v[120:123], v[72:79], v112
	s_waitcnt lgkmcnt(0)
	s_cmp_eq_u32 s26, 7
	s_cbranch_scc1 .Lgru2_nopf
	s_add_u32 s22, s22, s27
	s_addc_u32 s23, s23, s50
	s_add_u32 s46, s46, s27
	s_addc_u32 s47, s47, s50
	s_add_u32 s24, s24, s27
	s_addc_u32 s25, s25, s50
	s_add_u32 s48, s48, s27
	s_addc_u32 s49, s49, s50
	global_load_dwordx2 v[176:177], v172, s[22:23] offset:0
	global_load_dwordx2 v[178:179], v172, s[22:23] offset:512
	global_load_dwordx2 v[180:181], v172, s[22:23] offset:1024
	global_load_dwordx2 v[192:193], v172, s[24:25] offset:0
	global_load_dwordx2 v[194:195], v172, s[24:25] offset:512
	global_load_dwordx2 v[196:197], v172, s[24:25] offset:1024
	global_load_dwordx2 v[184:185], v172, s[46:47] offset:0
	global_load_dwordx2 v[186:187], v172, s[46:47] offset:512
	global_load_dwordx2 v[188:189], v172, s[46:47] offset:1024
	global_load_dwordx2 v[200:201], v172, s[48:49] offset:0
	global_load_dwordx2 v[202:203], v172, s[48:49] offset:512
	global_load_dwordx2 v[204:205], v172, s[48:49] offset:1024
	global_load_dwordx2 v[182:183], v114, s[22:23] offset:1536
	global_load_dwordx2 v[198:199], v114, s[24:25] offset:1536
	global_load_dwordx2 v[190:191], v114, s[46:47] offset:1536
	global_load_dwordx2 v[206:207], v114, s[48:49] offset:1536
.Lgru2_nopf:
	v_smfmac_f32_16x16x64_f16 v[136:139], v[124:127], v[32:39], v112
	v_smfmac_f32_16x16x64_f16 v[148:151], v[124:127], v[104:111], v112
	v_smfmac_f32_16x16x64_f16 v[140:143], v[124:127], v[56:63], v112
	v_smfmac_f32_16x16x64_f16 v[144:147], v[124:127], v[80:87], v112
	s_nop 8
	v_add_f32_e32 v153, v136, v137
	v_add_f32_e32 v156, v148, v149
	v_add_f32_e32 v154, v140, v141
	v_add_f32_e32 v155, v144, v145
	v_mov_b32_dpp v157, v156 row_shl:3 row_mask:0xf bank_mask:0xf bound_ctrl:1
	v_mov_b32_dpp v158, v156 row_shl:6 row_mask:0xf bank_mask:0xf bound_ctrl:1
	v_cndmask_b32_e64 v159, v156, v153, s[28:29]
	v_exp_f32_e32 v159, v159
	v_cndmask_b32_e64 v160, v157, v154, s[28:29]
	v_exp_f32_e32 v160, v160
	v_cndmask_b32_e64 v155, v158, v155, s[28:29]
	v_add_f32_e32 v159, 1.0, v159
	v_rcp_f32_e32 v159, v159
	v_add_f32_e32 v160, 1.0, v160
	v_rcp_f32_e32 v160, v160
	v_fmac_f32_e32 v152, v159, v155
	v_exp_f32_e32 v152, v152
	ds_read_b32 v136, v163 offset:3840
	ds_read_b32 v140, v164 offset:3840
	ds_read_b32 v148, v165 offset:3840
	v_mov_b32_e32 v144, v113
	v_mov_b32_e32 v137, 0
	v_mov_b32_e32 v141, 0
	v_mov_b32_e32 v145, 0
	v_mov_b32_e32 v149, 0
	v_add_f32_e32 v152, 1.0, v152
	v_rcp_f32_e32 v159, v152
	s_nop 0
	v_fma_f32 v159, v159, -2.0, 1.0
	ds_read_b32 v152, v166 offset:3840
	v_sub_f32_e32 v153, v161, v159
	v_fma_mixlo_f16 v162, v160, v153, v159
	v_fma_f32 v161, v160, v153, v159
	ds_write_b16 v168, v162 offset:0
	global_store_dword v[170:171], v161, off
	v_lshl_add_u64 v[170:171], v[170:171], 0, s[20:21]
	s_waitcnt lgkmcnt(0)
	s_barrier
	ds_read_b128 v[116:119], v167 offset:0
	ds_read_b128 v[120:123], v167 offset:128
	ds_read_b128 v[124:127], v167 offset:256
	s_waitcnt lgkmcnt(2)
	v_smfmac_f32_16x16x64_f16 v[136:139], v[116:119], v[16:23], v112
	v_smfmac_f32_16x16x64_f16 v[148:151], v[116:119], v[88:95], v112
	v_smfmac_f32_16x16x64_f16 v[140:143], v[116:119], v[40:47], v112
	v_smfmac_f32_16x16x64_f16 v[144:147], v[116:119], v[64:71], v112
	s_waitcnt lgkmcnt(1)
	v_smfmac_f32_16x16x64_f16 v[136:139], v[120:123], v[24:31], v112
	v_smfmac_f32_16x16x64_f16 v[148:151], v[120:123], v[96:103], v112
	v_smfmac_f32_16x16x64_f16 v[140:143], v[120:123], v[48:55], v112
	v_smfmac_f32_16x16x64_f16 v[144:147], v[120:123], v[72:79], v112
	s_waitcnt lgkmcnt(0)
	v_smfmac_f32_16x16x64_f16 v[136:139], v[124:127], v[32:39], v112
	v_smfmac_f32_16x16x64_f16 v[148:151], v[124:127], v[104:111], v112
	v_smfmac_f32_16x16x64_f16 v[140:143], v[124:127], v[56:63], v112
	v_smfmac_f32_16x16x64_f16 v[144:147], v[124:127], v[80:87], v112
	s_nop 8
	v_add_f32_e32 v153, v136, v137
	v_add_f32_e32 v156, v148, v149
	v_add_f32_e32 v154, v140, v141
	v_add_f32_e32 v155, v144, v145
	v_mov_b32_dpp v157, v156 row_shl:3 row_mask:0xf bank_mask:0xf bound_ctrl:1
	v_mov_b32_dpp v158, v156 row_shl:6 row_mask:0xf bank_mask:0xf bound_ctrl:1
	v_cndmask_b32_e64 v159, v156, v153, s[28:29]
	v_exp_f32_e32 v159, v159
	v_cndmask_b32_e64 v160, v157, v154, s[28:29]
	v_exp_f32_e32 v160, v160
	v_cndmask_b32_e64 v155, v158, v155, s[28:29]
	v_add_f32_e32 v159, 1.0, v159
	v_rcp_f32_e32 v159, v159
	v_add_f32_e32 v160, 1.0, v160
	v_rcp_f32_e32 v160, v160
	v_fmac_f32_e32 v152, v159, v155
	v_exp_f32_e32 v152, v152
	ds_read_b32 v136, v163 offset:5760
	ds_read_b32 v140, v164 offset:5760
	ds_read_b32 v148, v165 offset:5760
	v_mov_b32_e32 v144, v113
	v_mov_b32_e32 v137, 0
	v_mov_b32_e32 v141, 0
	v_mov_b32_e32 v145, 0
	v_mov_b32_e32 v149, 0
	v_add_f32_e32 v152, 1.0, v152
	v_rcp_f32_e32 v159, v152
	s_nop 0
	v_fma_f32 v159, v159, -2.0, 1.0
	ds_read_b32 v152, v166 offset:5760
	v_sub_f32_e32 v153, v161, v159
	v_fma_mixlo_f16 v162, v160, v153, v159
	v_fma_f32 v161, v160, v153, v159
	ds_write_b16 v168, v162 offset:384
	global_store_dword v[170:171], v161, off
	v_lshl_add_u64 v[170:171], v[170:171], 0, s[20:21]
	s_waitcnt lgkmcnt(0)
	s_barrier
	ds_read_b128 v[116:119], v167 offset:384
	ds_read_b128 v[120:123], v167 offset:512
	ds_read_b128 v[124:127], v167 offset:640
	s_waitcnt lgkmcnt(2)
	v_smfmac_f32_16x16x64_f16 v[136:139], v[116:119], v[16:23], v112
	v_smfmac_f32_16x16x64_f16 v[148:151], v[116:119], v[88:95], v112
	v_smfmac_f32_16x16x64_f16 v[140:143], v[116:119], v[40:47], v112
	v_smfmac_f32_16x16x64_f16 v[144:147], v[116:119], v[64:71], v112
	s_waitcnt lgkmcnt(1)
	v_smfmac_f32_16x16x64_f16 v[136:139], v[120:123], v[24:31], v112
	v_smfmac_f32_16x16x64_f16 v[148:151], v[120:123], v[96:103], v112
	v_smfmac_f32_16x16x64_f16 v[140:143], v[120:123], v[48:55], v112
	v_smfmac_f32_16x16x64_f16 v[144:147], v[120:123], v[72:79], v112
	s_waitcnt lgkmcnt(0)
	v_smfmac_f32_16x16x64_f16 v[136:139], v[124:127], v[32:39], v112
	v_smfmac_f32_16x16x64_f16 v[148:151], v[124:127], v[104:111], v112
	v_smfmac_f32_16x16x64_f16 v[140:143], v[124:127], v[56:63], v112
	v_smfmac_f32_16x16x64_f16 v[144:147], v[124:127], v[80:87], v112
	s_nop 8
	v_add_f32_e32 v153, v136, v137
	v_add_f32_e32 v156, v148, v149
	v_add_f32_e32 v154, v140, v141
	v_add_f32_e32 v155, v144, v145
	v_mov_b32_dpp v157, v156 row_shl:3 row_mask:0xf bank_mask:0xf bound_ctrl:1
	v_mov_b32_dpp v158, v156 row_shl:6 row_mask:0xf bank_mask:0xf bound_ctrl:1
	v_cndmask_b32_e64 v159, v156, v153, s[28:29]
	v_exp_f32_e32 v159, v159
	v_cndmask_b32_e64 v160, v157, v154, s[28:29]
	v_exp_f32_e32 v160, v160
	v_cndmask_b32_e64 v155, v158, v155, s[28:29]
	v_add_f32_e32 v159, 1.0, v159
	v_rcp_f32_e32 v159, v159
	v_add_f32_e32 v160, 1.0, v160
	v_rcp_f32_e32 v160, v160
	v_fmac_f32_e32 v152, v159, v155
	v_exp_f32_e32 v152, v152
	ds_read_b32 v136, v163 offset:7680
	ds_read_b32 v140, v164 offset:7680
	ds_read_b32 v148, v165 offset:7680
	v_mov_b32_e32 v144, v113
	v_mov_b32_e32 v137, 0
	v_mov_b32_e32 v141, 0
	v_mov_b32_e32 v145, 0
	v_mov_b32_e32 v149, 0
	v_add_f32_e32 v152, 1.0, v152
	v_rcp_f32_e32 v159, v152
	s_nop 0
	v_fma_f32 v159, v159, -2.0, 1.0
	ds_read_b32 v152, v166 offset:7680
	v_sub_f32_e32 v153, v161, v159
	v_fma_mixlo_f16 v162, v160, v153, v159
	v_fma_f32 v161, v160, v153, v159
	ds_write_b16 v168, v162 offset:0
	global_store_dword v[170:171], v161, off
	v_lshl_add_u64 v[170:171], v[170:171], 0, s[20:21]
	s_waitcnt lgkmcnt(0)
	s_barrier
	ds_read_b128 v[116:119], v167 offset:0
	ds_read_b128 v[120:123], v167 offset:128
	ds_read_b128 v[124:127], v167 offset:256
	s_waitcnt lgkmcnt(2)
	v_smfmac_f32_16x16x64_f16 v[136:139], v[116:119], v[16:23], v112
	v_smfmac_f32_16x16x64_f16 v[148:151], v[116:119], v[88:95], v112
	v_smfmac_f32_16x16x64_f16 v[140:143], v[116:119], v[40:47], v112
	v_smfmac_f32_16x16x64_f16 v[144:147], v[116:119], v[64:71], v112
	s_waitcnt lgkmcnt(1)
	v_smfmac_f32_16x16x64_f16 v[136:139], v[120:123], v[24:31], v112
	v_smfmac_f32_16x16x64_f16 v[148:151], v[120:123], v[96:103], v112
	v_smfmac_f32_16x16x64_f16 v[140:143], v[120:123], v[48:55], v112
	v_smfmac_f32_16x16x64_f16 v[144:147], v[120:123], v[72:79], v112
	s_waitcnt lgkmcnt(0)
	v_smfmac_f32_16x16x64_f16 v[136:139], v[124:127], v[32:39], v112
	v_smfmac_f32_16x16x64_f16 v[148:151], v[124:127], v[104:111], v112
	v_smfmac_f32_16x16x64_f16 v[140:143], v[124:127], v[56:63], v112
	v_smfmac_f32_16x16x64_f16 v[144:147], v[124:127], v[80:87], v112
	s_nop 8
	v_add_f32_e32 v153, v136, v137
	v_add_f32_e32 v156, v148, v149
	v_add_f32_e32 v154, v140, v141
	v_add_f32_e32 v155, v144, v145
	v_mov_b32_dpp v157, v156 row_shl:3 row_mask:0xf bank_mask:0xf bound_ctrl:1
	v_mov_b32_dpp v158, v156 row_shl:6 row_mask:0xf bank_mask:0xf bound_ctrl:1
	v_cndmask_b32_e64 v159, v156, v153, s[28:29]
	v_exp_f32_e32 v159, v159
	v_cndmask_b32_e64 v160, v157, v154, s[28:29]
	v_exp_f32_e32 v160, v160
	v_cndmask_b32_e64 v155, v158, v155, s[28:29]
	v_add_f32_e32 v159, 1.0, v159
	v_rcp_f32_e32 v159, v159
	v_add_f32_e32 v160, 1.0, v160
	v_rcp_f32_e32 v160, v160
	v_fmac_f32_e32 v152, v159, v155
	v_exp_f32_e32 v152, v152
	ds_read_b32 v136, v163 offset:9600
	ds_read_b32 v140, v164 offset:9600
	ds_read_b32 v148, v165 offset:9600
	v_mov_b32_e32 v144, v113
	v_mov_b32_e32 v137, 0
	v_mov_b32_e32 v141, 0
	v_mov_b32_e32 v145, 0
	v_mov_b32_e32 v149, 0
	v_add_f32_e32 v152, 1.0, v152
	v_rcp_f32_e32 v159, v152
	s_nop 0
	v_fma_f32 v159, v159, -2.0, 1.0
	ds_read_b32 v152, v166 offset:9600
	v_sub_f32_e32 v153, v161, v159
	v_fma_mixlo_f16 v162, v160, v153, v159
	v_fma_f32 v161, v160, v153, v159
	ds_write_b16 v168, v162 offset:384
	global_store_dword v[170:171], v161, off
	v_lshl_add_u64 v[170:171], v[170:171], 0, s[20:21]
	s_waitcnt lgkmcnt(0)
	s_barrier
	ds_read_b128 v[116:119], v167 offset:384
	ds_read_b128 v[120:123], v167 offset:512
	ds_read_b128 v[124:127], v167 offset:640
	s_waitcnt lgkmcnt(2)
	v_smfmac_f32_16x16x64_f16 v[136:139], v[116:119], v[16:23], v112
	v_smfmac_f32_16x16x64_f16 v[148:151], v[116:119], v[88:95], v112
	v_smfmac_f32_16x16x64_f16 v[140:143], v[116:119], v[40:47], v112
	v_smfmac_f32_16x16x64_f16 v[144:147], v[116:119], v[64:71], v112
	s_waitcnt lgkmcnt(1)
	v_smfmac_f32_16x16x64_f16 v[136:139], v[120:123], v[24:31], v112
	v_smfmac_f32_16x16x64_f16 v[148:151], v[120:123], v[96:103], v112
	v_smfmac_f32_16x16x64_f16 v[140:143], v[120:123], v[48:55], v112
	v_smfmac_f32_16x16x64_f16 v[144:147], v[120:123], v[72:79], v112
	s_waitcnt lgkmcnt(0)
	v_smfmac_f32_16x16x64_f16 v[136:139], v[124:127], v[32:39], v112
	v_smfmac_f32_16x16x64_f16 v[148:151], v[124:127], v[104:111], v112
	v_smfmac_f32_16x16x64_f16 v[140:143], v[124:127], v[56:63], v112
	v_smfmac_f32_16x16x64_f16 v[144:147], v[124:127], v[80:87], v112
	s_nop 8
	v_add_f32_e32 v153, v136, v137
	v_add_f32_e32 v156, v148, v149
	v_add_f32_e32 v154, v140, v141
	v_add_f32_e32 v155, v144, v145
	v_mov_b32_dpp v157, v156 row_shl:3 row_mask:0xf bank_mask:0xf bound_ctrl:1
	v_mov_b32_dpp v158, v156 row_shl:6 row_mask:0xf bank_mask:0xf bound_ctrl:1
	v_cndmask_b32_e64 v159, v156, v153, s[28:29]
	v_exp_f32_e32 v159, v159
	v_cndmask_b32_e64 v160, v157, v154, s[28:29]
	v_exp_f32_e32 v160, v160
	v_cndmask_b32_e64 v155, v158, v155, s[28:29]
	v_add_f32_e32 v159, 1.0, v159
	v_rcp_f32_e32 v159, v159
	v_add_f32_e32 v160, 1.0, v160
	v_rcp_f32_e32 v160, v160
	v_fmac_f32_e32 v152, v159, v155
	v_exp_f32_e32 v152, v152
	ds_read_b32 v136, v163 offset:11520
	ds_read_b32 v140, v164 offset:11520
	ds_read_b32 v148, v165 offset:11520
	v_mov_b32_e32 v144, v113
	v_mov_b32_e32 v137, 0
	v_mov_b32_e32 v141, 0
	v_mov_b32_e32 v145, 0
	v_mov_b32_e32 v149, 0
	v_add_f32_e32 v152, 1.0, v152
	v_rcp_f32_e32 v159, v152
	s_nop 0
	v_fma_f32 v159, v159, -2.0, 1.0
	ds_read_b32 v152, v166 offset:11520
	v_sub_f32_e32 v153, v161, v159
	v_fma_mixlo_f16 v162, v160, v153, v159
	v_fma_f32 v161, v160, v153, v159
	ds_write_b16 v168, v162 offset:0
	global_store_dword v[170:171], v161, off
	v_lshl_add_u64 v[170:171], v[170:171], 0, s[20:21]
	s_waitcnt lgkmcnt(0)
	s_barrier
	ds_read_b128 v[116:119], v167 offset:0
	ds_read_b128 v[120:123], v167 offset:128
	ds_read_b128 v[124:127], v167 offset:256
	s_waitcnt lgkmcnt(2)
	v_smfmac_f32_16x16x64_f16 v[136:139], v[116:119], v[16:23], v112
	v_smfmac_f32_16x16x64_f16 v[148:151], v[116:119], v[88:95], v112
	v_smfmac_f32_16x16x64_f16 v[140:143], v[116:119], v[40:47], v112
	v_smfmac_f32_16x16x64_f16 v[144:147], v[116:119], v[64:71], v112
	s_waitcnt lgkmcnt(1)
	v_smfmac_f32_16x16x64_f16 v[136:139], v[120:123], v[24:31], v112
	v_smfmac_f32_16x16x64_f16 v[148:151], v[120:123], v[96:103], v112
	v_smfmac_f32_16x16x64_f16 v[140:143], v[120:123], v[48:55], v112
	v_smfmac_f32_16x16x64_f16 v[144:147], v[120:123], v[72:79], v112
	s_waitcnt lgkmcnt(0)
	v_smfmac_f32_16x16x64_f16 v[136:139], v[124:127], v[32:39], v112
	v_smfmac_f32_16x16x64_f16 v[148:151], v[124:127], v[104:111], v112
	v_smfmac_f32_16x16x64_f16 v[140:143], v[124:127], v[56:63], v112
	v_smfmac_f32_16x16x64_f16 v[144:147], v[124:127], v[80:87], v112
	s_nop 8
	v_add_f32_e32 v153, v136, v137
	v_add_f32_e32 v156, v148, v149
	v_add_f32_e32 v154, v140, v141
	v_add_f32_e32 v155, v144, v145
	v_mov_b32_dpp v157, v156 row_shl:3 row_mask:0xf bank_mask:0xf bound_ctrl:1
	v_mov_b32_dpp v158, v156 row_shl:6 row_mask:0xf bank_mask:0xf bound_ctrl:1
	v_cndmask_b32_e64 v159, v156, v153, s[28:29]
	v_exp_f32_e32 v159, v159
	v_cndmask_b32_e64 v160, v157, v154, s[28:29]
	v_exp_f32_e32 v160, v160
	v_cndmask_b32_e64 v155, v158, v155, s[28:29]
	v_add_f32_e32 v159, 1.0, v159
	v_rcp_f32_e32 v159, v159
	v_add_f32_e32 v160, 1.0, v160
	v_rcp_f32_e32 v160, v160
	v_fmac_f32_e32 v152, v159, v155
	v_exp_f32_e32 v152, v152
	ds_read_b32 v136, v163 offset:13440
	ds_read_b32 v140, v164 offset:13440
	ds_read_b32 v148, v165 offset:13440
	v_mov_b32_e32 v144, v113
	v_mov_b32_e32 v137, 0
	v_mov_b32_e32 v141, 0
	v_mov_b32_e32 v145, 0
	v_mov_b32_e32 v149, 0
	v_add_f32_e32 v152, 1.0, v152
	v_rcp_f32_e32 v159, v152
	s_nop 0
	v_fma_f32 v159, v159, -2.0, 1.0
	ds_read_b32 v152, v166 offset:13440
	v_sub_f32_e32 v153, v161, v159
	v_fma_mixlo_f16 v162, v160, v153, v159
	v_fma_f32 v161, v160, v153, v159
	ds_write_b16 v168, v162 offset:384
	global_store_dword v[170:171], v161, off
	v_lshl_add_u64 v[170:171], v[170:171], 0, s[20:21]
	s_waitcnt lgkmcnt(0)
	s_barrier
	ds_read_b128 v[116:119], v167 offset:384
	ds_read_b128 v[120:123], v167 offset:512
	ds_read_b128 v[124:127], v167 offset:640
	s_waitcnt lgkmcnt(2)
	v_smfmac_f32_16x16x64_f16 v[136:139], v[116:119], v[16:23], v112
	v_smfmac_f32_16x16x64_f16 v[148:151], v[116:119], v[88:95], v112
	v_smfmac_f32_16x16x64_f16 v[140:143], v[116:119], v[40:47], v112
	v_smfmac_f32_16x16x64_f16 v[144:147], v[116:119], v[64:71], v112
	s_waitcnt lgkmcnt(1)
	v_smfmac_f32_16x16x64_f16 v[136:139], v[120:123], v[24:31], v112
	v_smfmac_f32_16x16x64_f16 v[148:151], v[120:123], v[96:103], v112
	v_smfmac_f32_16x16x64_f16 v[140:143], v[120:123], v[48:55], v112
	v_smfmac_f32_16x16x64_f16 v[144:147], v[120:123], v[72:79], v112
	s_waitcnt lgkmcnt(0)
	v_smfmac_f32_16x16x64_f16 v[136:139], v[124:127], v[32:39], v112
	v_smfmac_f32_16x16x64_f16 v[148:151], v[124:127], v[104:111], v112
	v_smfmac_f32_16x16x64_f16 v[140:143], v[124:127], v[56:63], v112
	v_smfmac_f32_16x16x64_f16 v[144:147], v[124:127], v[80:87], v112
	s_nop 8
	v_add_f32_e32 v153, v136, v137
	v_add_f32_e32 v156, v148, v149
	v_add_f32_e32 v154, v140, v141
	v_add_f32_e32 v155, v144, v145
	v_mov_b32_dpp v157, v156 row_shl:3 row_mask:0xf bank_mask:0xf bound_ctrl:1
	v_mov_b32_dpp v158, v156 row_shl:6 row_mask:0xf bank_mask:0xf bound_ctrl:1
	v_cndmask_b32_e64 v159, v156, v153, s[28:29]
	v_exp_f32_e32 v159, v159
	v_cndmask_b32_e64 v160, v157, v154, s[28:29]
	v_exp_f32_e32 v160, v160
	v_cndmask_b32_e64 v155, v158, v155, s[28:29]
	v_add_f32_e32 v159, 1.0, v159
	v_rcp_f32_e32 v159, v159
	v_add_f32_e32 v160, 1.0, v160
	v_rcp_f32_e32 v160, v160
	v_fmac_f32_e32 v152, v159, v155
	v_exp_f32_e32 v152, v152
	ds_read_b32 v136, v163 offset:15360
	ds_read_b32 v140, v164 offset:15360
	ds_read_b32 v148, v165 offset:15360
	v_mov_b32_e32 v144, v113
	v_mov_b32_e32 v137, 0
	v_mov_b32_e32 v141, 0
	v_mov_b32_e32 v145, 0
	v_mov_b32_e32 v149, 0
	v_add_f32_e32 v152, 1.0, v152
	v_rcp_f32_e32 v159, v152
	s_nop 0
	v_fma_f32 v159, v159, -2.0, 1.0
	ds_read_b32 v152, v166 offset:15360
	v_sub_f32_e32 v153, v161, v159
	v_fma_mixlo_f16 v162, v160, v153, v159
	v_fma_f32 v161, v160, v153, v159
	ds_write_b16 v168, v162 offset:0
	global_store_dword v[170:171], v161, off
	v_lshl_add_u64 v[170:171], v[170:171], 0, s[20:21]
	s_waitcnt lgkmcnt(0)
	s_barrier
	ds_read_b128 v[116:119], v167 offset:0
	ds_read_b128 v[120:123], v167 offset:128
	ds_read_b128 v[124:127], v167 offset:256
	s_waitcnt lgkmcnt(2)
	v_smfmac_f32_16x16x64_f16 v[136:139], v[116:119], v[16:23], v112
	v_smfmac_f32_16x16x64_f16 v[148:151], v[116:119], v[88:95], v112
	v_smfmac_f32_16x16x64_f16 v[140:143], v[116:119], v[40:47], v112
	v_smfmac_f32_16x16x64_f16 v[144:147], v[116:119], v[64:71], v112
	s_waitcnt lgkmcnt(1)
	v_smfmac_f32_16x16x64_f16 v[136:139], v[120:123], v[24:31], v112
	v_smfmac_f32_16x16x64_f16 v[148:151], v[120:123], v[96:103], v112
	v_smfmac_f32_16x16x64_f16 v[140:143], v[120:123], v[48:55], v112
	v_smfmac_f32_16x16x64_f16 v[144:147], v[120:123], v[72:79], v112
	s_waitcnt lgkmcnt(0)
	v_smfmac_f32_16x16x64_f16 v[136:139], v[124:127], v[32:39], v112
	v_smfmac_f32_16x16x64_f16 v[148:151], v[124:127], v[104:111], v112
	v_smfmac_f32_16x16x64_f16 v[140:143], v[124:127], v[56:63], v112
	v_smfmac_f32_16x16x64_f16 v[144:147], v[124:127], v[80:87], v112
	s_nop 8
	v_add_f32_e32 v153, v136, v137
	v_add_f32_e32 v156, v148, v149
	v_add_f32_e32 v154, v140, v141
	v_add_f32_e32 v155, v144, v145
	v_mov_b32_dpp v157, v156 row_shl:3 row_mask:0xf bank_mask:0xf bound_ctrl:1
	v_mov_b32_dpp v158, v156 row_shl:6 row_mask:0xf bank_mask:0xf bound_ctrl:1
	v_cndmask_b32_e64 v159, v156, v153, s[28:29]
	v_exp_f32_e32 v159, v159
	v_cndmask_b32_e64 v160, v157, v154, s[28:29]
	v_exp_f32_e32 v160, v160
	v_cndmask_b32_e64 v155, v158, v155, s[28:29]
	v_add_f32_e32 v159, 1.0, v159
	v_rcp_f32_e32 v159, v159
	v_add_f32_e32 v160, 1.0, v160
	v_rcp_f32_e32 v160, v160
	v_fmac_f32_e32 v152, v159, v155
	v_exp_f32_e32 v152, v152
	ds_read_b32 v136, v163 offset:17280
	ds_read_b32 v140, v164 offset:17280
	ds_read_b32 v148, v165 offset:17280
	v_mov_b32_e32 v144, v113
	v_mov_b32_e32 v137, 0
	v_mov_b32_e32 v141, 0
	v_mov_b32_e32 v145, 0
	v_mov_b32_e32 v149, 0
	v_add_f32_e32 v152, 1.0, v152
	v_rcp_f32_e32 v159, v152
	s_nop 0
	v_fma_f32 v159, v159, -2.0, 1.0
	ds_read_b32 v152, v166 offset:17280
	v_sub_f32_e32 v153, v161, v159
	v_fma_mixlo_f16 v162, v160, v153, v159
	v_fma_f32 v161, v160, v153, v159
	ds_write_b16 v168, v162 offset:384
	global_store_dword v[170:171], v161, off
	v_lshl_add_u64 v[170:171], v[170:171], 0, s[20:21]
	s_waitcnt lgkmcnt(0)
	s_barrier
	ds_read_b128 v[116:119], v167 offset:384
	ds_read_b128 v[120:123], v167 offset:512
	ds_read_b128 v[124:127], v167 offset:640
	s_waitcnt lgkmcnt(2)
	v_smfmac_f32_16x16x64_f16 v[136:139], v[116:119], v[16:23], v112
	v_smfmac_f32_16x16x64_f16 v[148:151], v[116:119], v[88:95], v112
	v_smfmac_f32_16x16x64_f16 v[140:143], v[116:119], v[40:47], v112
	v_smfmac_f32_16x16x64_f16 v[144:147], v[116:119], v[64:71], v112
	s_waitcnt lgkmcnt(1)
	v_smfmac_f32_16x16x64_f16 v[136:139], v[120:123], v[24:31], v112
	v_smfmac_f32_16x16x64_f16 v[148:151], v[120:123], v[96:103], v112
	v_smfmac_f32_16x16x64_f16 v[140:143], v[120:123], v[48:55], v112
	v_smfmac_f32_16x16x64_f16 v[144:147], v[120:123], v[72:79], v112
	s_waitcnt lgkmcnt(0)
	s_cmp_eq_u32 s26, 7
	s_cbranch_scc1 .Lgru2_nost0
	s_waitcnt vmcnt(4)
	v_add_f32_e32 v176, v176, v192
	v_add_f32_e32 v177, v177, v193
	v_mul_f32_e32 v176, s51, v176
	v_mul_f32_e32 v177, s51, v177
	v_add_f32_e32 v178, v178, v194
	v_add_f32_e32 v179, v179, v195
	v_mul_f32_e32 v178, s51, v178
	v_mul_f32_e32 v179, s51, v179
	v_add_f32_e32 v180, v180, v196
	v_add_f32_e32 v181, v181, v197
	v_mul_f32_e32 v180, v175, v180
	v_mul_f32_e32 v181, v175, v181
	v_add_f32_e32 v182, v182, v198
	v_add_f32_e32 v183, v183, v199
	v_mul_f32_e32 v182, s52, v182
	v_mul_f32_e32 v183, s52, v183
	ds_write_b64 v173, v[176:177] offset:0
	ds_write_b64 v173, v[178:179] offset:512
	ds_write_b64 v173, v[180:181] offset:1024
	ds_write_b64 v115, v[182:183] offset:1536
.Lgru2_nost0:
	v_smfmac_f32_16x16x64_f16 v[136:139], v[124:127], v[32:39], v112
	v_smfmac_f32_16x16x64_f16 v[148:151], v[124:127], v[104:111], v112
	v_smfmac_f32_16x16x64_f16 v[140:143], v[124:127], v[56:63], v112
	v_smfmac_f32_16x16x64_f16 v[144:147], v[124:127], v[80:87], v112
	s_nop 8
	v_add_f32_e32 v153, v136, v137
	v_add_f32_e32 v156, v148, v149
	v_add_f32_e32 v154, v140, v141
	v_add_f32_e32 v155, v144, v145
	v_mov_b32_dpp v157, v156 row_shl:3 row_mask:0xf bank_mask:0xf bound_ctrl:1
	v_mov_b32_dpp v158, v156 row_shl:6 row_mask:0xf bank_mask:0xf bound_ctrl:1
	v_cndmask_b32_e64 v159, v156, v153, s[28:29]
	v_exp_f32_e32 v159, v159
	v_cndmask_b32_e64 v160, v157, v154, s[28:29]
	v_exp_f32_e32 v160, v160
	v_cndmask_b32_e64 v155, v158, v155, s[28:29]
	v_add_f32_e32 v159, 1.0, v159
	v_rcp_f32_e32 v159, v159
	v_add_f32_e32 v160, 1.0, v160
	v_rcp_f32_e32 v160, v160
	v_fmac_f32_e32 v152, v159, v155
	v_exp_f32_e32 v152, v152
	ds_read_b32 v136, v163 offset:19200
	ds_read_b32 v140, v164 offset:19200
	ds_read_b32 v148, v165 offset:19200
	v_mov_b32_e32 v144, v113
	v_mov_b32_e32 v137, 0
	v_mov_b32_e32 v141, 0
	v_mov_b32_e32 v145, 0
	v_mov_b32_e32 v149, 0
	v_add_f32_e32 v152, 1.0, v152
	v_rcp_f32_e32 v159, v152
	s_nop 0
	v_fma_f32 v159, v159, -2.0, 1.0
	ds_read_b32 v152, v166 offset:19200
	v_sub_f32_e32 v153, v161, v159
	v_fma_mixlo_f16 v162, v160, v153, v159
	v_fma_f32 v161, v160, v153, v159
	ds_write_b16 v168, v162 offset:0
	global_store_dword v[170:171], v161, off
	v_lshl_add_u64 v[170:171], v[170:171], 0, s[20:21]
	s_waitcnt lgkmcnt(0)
	s_barrier
	ds_read_b128 v[116:119], v167 offset:0
	ds_read_b128 v[120:123], v167 offset:128
	ds_read_b128 v[124:127], v167 offset:256
	s_waitcnt lgkmcnt(2)
	v_smfmac_f32_16x16x64_f16 v[136:139], v[116:119], v[16:23], v112
	v_smfmac_f32_16x16x64_f16 v[148:151], v[116:119], v[88:95], v112
	v_smfmac_f32_16x16x64_f16 v[140:143], v[116:119], v[40:47], v112
	v_smfmac_f32_16x16x64_f16 v[144:147], v[116:119], v[64:71], v112
	s_waitcnt lgkmcnt(1)
	v_smfmac_f32_16x16x64_f16 v[136:139], v[120:123], v[24:31], v112
	v_smfmac_f32_16x16x64_f16 v[148:151], v[120:123], v[96:103], v112
	v_smfmac_f32_16x16x64_f16 v[140:143], v[120:123], v[48:55], v112
	v_smfmac_f32_16x16x64_f16 v[144:147], v[120:123], v[72:79], v112
	s_waitcnt lgkmcnt(0)
	v_smfmac_f32_16x16x64_f16 v[136:139], v[124:127], v[32:39], v112
	v_smfmac_f32_16x16x64_f16 v[148:151], v[124:127], v[104:111], v112
	v_smfmac_f32_16x16x64_f16 v[140:143], v[124:127], v[56:63], v112
	v_smfmac_f32_16x16x64_f16 v[144:147], v[124:127], v[80:87], v112
	s_nop 8
	v_add_f32_e32 v153, v136, v137
	v_add_f32_e32 v156, v148, v149
	v_add_f32_e32 v154, v140, v141
	v_add_f32_e32 v155, v144, v145
	v_mov_b32_dpp v157, v156 row_shl:3 row_mask:0xf bank_mask:0xf bound_ctrl:1
	v_mov_b32_dpp v158, v156 row_shl:6 row_mask:0xf bank_mask:0xf bound_ctrl:1
	v_cndmask_b32_e64 v159, v156, v153, s[28:29]
	v_exp_f32_e32 v159, v159
	v_cndmask_b32_e64 v160, v157, v154, s[28:29]
	v_exp_f32_e32 v160, v160
	v_cndmask_b32_e64 v155, v158, v155, s[28:29]
	v_add_f32_e32 v159, 1.0, v159
	v_rcp_f32_e32 v159, v159
	v_add_f32_e32 v160, 1.0, v160
	v_rcp_f32_e32 v160, v160
	v_fmac_f32_e32 v152, v159, v155
	v_exp_f32_e32 v152, v152
	ds_read_b32 v136, v163 offset:21120
	ds_read_b32 v140, v164 offset:21120
	ds_read_b32 v148, v165 offset:21120
	v_mov_b32_e32 v144, v113
	v_mov_b32_e32 v137, 0
	v_mov_b32_e32 v141, 0
	v_mov_b32_e32 v145, 0
	v_mov_b32_e32 v149, 0
	v_add_f32_e32 v152, 1.0, v152
	v_rcp_f32_e32 v159, v152
	s_nop 0
	v_fma_f32 v159, v159, -2.0, 1.0
	ds_read_b32 v152, v166 offset:21120
	v_sub_f32_e32 v153, v161, v159
	v_fma_mixlo_f16 v162, v160, v153, v159
	v_fma_f32 v161, v160, v153, v159
	ds_write_b16 v168, v162 offset:384
	global_store_dword v[170:171], v161, off
	v_lshl_add_u64 v[170:171], v[170:171], 0, s[20:21]
	s_waitcnt lgkmcnt(0)
	s_barrier
	ds_read_b128 v[116:119], v167 offset:384
	ds_read_b128 v[120:123], v167 offset:512
	ds_read_b128 v[124:127], v167 offset:640
	s_waitcnt lgkmcnt(2)
	v_smfmac_f32_16x16x64_f16 v[136:139], v[116:119], v[16:23], v112
	v_smfmac_f32_16x16x64_f16 v[148:151], v[116:119], v[88:95], v112
	v_smfmac_f32_16x16x64_f16 v[140:143], v[116:119], v[40:47], v112
	v_smfmac_f32_16x16x64_f16 v[144:147], v[116:119], v[64:71], v112
	s_waitcnt lgkmcnt(1)
	v_smfmac_f32_16x16x64_f16 v[136:139], v[120:123], v[24:31], v112
	v_smfmac_f32_16x16x64_f16 v[148:151], v[120:123], v[96:103], v112
	v_smfmac_f32_16x16x64_f16 v[140:143], v[120:123], v[48:55], v112
	v_smfmac_f32_16x16x64_f16 v[144:147], v[120:123], v[72:79], v112
	s_waitcnt lgkmcnt(0)
	s_cmp_eq_u32 s26, 7
	s_cbranch_scc1 .Lgru2_nost1
	s_waitcnt vmcnt(4)
	v_add_f32_e32 v184, v184, v200
	v_add_f32_e32 v185, v185, v201
	v_mul_f32_e32 v184, s51, v184
	v_mul_f32_e32 v185, s51, v185
	v_add_f32_e32 v186, v186, v202
	v_add_f32_e32 v187, v187, v203
	v_mul_f32_e32 v186, s51, v186
	v_mul_f32_e32 v187, s51, v187
	v_add_f32_e32 v188, v188, v204
	v_add_f32_e32 v189, v189, v205
	v_mul_f32_e32 v188, v175, v188
	v_mul_f32_e32 v189, v175, v189
	v_add_f32_e32 v190, v190, v206
	v_add_f32_e32 v191, v191, v207
	v_mul_f32_e32 v190, s52, v190
	v_mul_f32_e32 v191, s52, v191
	ds_write_b64 v174, v[184:185] offset:0
	ds_write_b64 v174, v[186:187] offset:512
	ds_write_b64 v174, v[188:189] offset:1024
	ds_write_b64 v169, v[190:191] offset:1536

	.text
	.p2alignl 8, 3212836864
	.fill 256, 4, 3212836864

amdhsa.kernels:
  - .agpr_count:     16
    .args:
      - .actual_access:  read_only
        .address_space:  global
        .offset:         0
        .size:           8
        .value_kind:     global_buffer
      - .actual_access:  read_only
        .address_space:  global
        .offset:         8
        .size:           8
        .value_kind:     global_buffer
      - .actual_access:  read_only
        .address_space:  global
        .offset:         16
        .size:           8
        .value_kind:     global_buffer
      - .actual_access:  read_only
        .address_space:  global
        .offset:         24
        .size:           8
        .value_kind:     global_buffer
      - .actual_access:  write_only
        .address_space:  global
        .offset:         32
        .size:           8
        .value_kind:     global_buffer
      - .offset:         40
        .size:           4
        .value_kind:     by_value
      - .offset:         44
        .size:           4
        .value_kind:     by_value
      - .offset:         48
        .size:           4
        .value_kind:     by_value
      - .offset:         52
        .size:           4
        .value_kind:     by_value
      - .offset:         56
        .size:           4
        .value_kind:     by_value
      - .offset:         60
        .size:           4
        .value_kind:     by_value
      - .offset:         64
        .size:           4
        .value_kind:     by_value
    .group_segment_fixed_size: 43008
    .kernarg_segment_align: 8
    .kernarg_segment_size: 68
    .language:       OpenCL C
    .language_version:
      - 2
      - 0
    .max_flat_workgroup_size: 256
    .name:           _Z15gemm_f16_kernelPKDF16_S0_PKfS2_Pfiiiiiii
    .private_segment_fixed_size: 0
    .sgpr_count:     33
    .sgpr_spill_count: 0
    .symbol:         _Z15gemm_f16_kernelPKDF16_S0_PKfS2_Pfiiiiiii.kd
    .uniform_work_group_size: 1
    .uses_dynamic_stack: false
    .vgpr_count:     104
    .vgpr_spill_count: 0
    .wavefront_size: 64
  - .agpr_count:     0
    .args:
      - .actual_access:  read_only
        .address_space:  global
        .offset:         0
        .size:           8
        .value_kind:     global_buffer
      - .actual_access:  read_only
        .address_space:  global
        .offset:         8
        .size:           8
        .value_kind:     global_buffer
      - .actual_access:  read_only
        .address_space:  global
        .offset:         16
        .size:           8
        .value_kind:     global_buffer
      - .actual_access:  read_only
        .address_space:  global
        .offset:         24
        .size:           8
        .value_kind:     global_buffer
      - .actual_access:  read_only
        .address_space:  global
        .offset:         32
        .size:           8
        .value_kind:     global_buffer
      - .actual_access:  read_only
        .address_space:  global
        .offset:         40
        .size:           8
        .value_kind:     global_buffer
      - .actual_access:  write_only
        .address_space:  global
        .offset:         48
        .size:           8
        .value_kind:     global_buffer
      - .actual_access:  read_only
        .address_space:  global
        .offset:         56
        .size:           8
        .value_kind:     global_buffer
    .group_segment_fixed_size: 121472
    .kernarg_segment_align: 8
    .kernarg_segment_size: 64
    .language:       OpenCL C
    .language_version:
      - 2
      - 0
    .max_flat_workgroup_size: 512
    .name:           _Z15score_ds_kernelPKfS0_S0_S0_S0_S0_PfPKDF16_
    .private_segment_fixed_size: 0
    .sgpr_count:     32
    .sgpr_spill_count: 0
    .symbol:         _Z15score_ds_kernelPKfS0_S0_S0_S0_S0_PfPKDF16_.kd
    .uniform_work_group_size: 1
    .uses_dynamic_stack: false
    .vgpr_count:     254
    .vgpr_spill_count: 0
    .wavefront_size: 64
  - .agpr_count:     0
    .args:
      - .actual_access:  read_only
        .address_space:  global
        .offset:         0
        .size:           8
        .value_kind:     global_buffer
      - .actual_access:  read_only
        .address_space:  global
        .offset:         8
        .size:           8
        .value_kind:     global_buffer
      - .actual_access:  read_only
        .address_space:  global
        .offset:         16
        .size:           8
        .value_kind:     global_buffer
      - .actual_access:  read_only
        .address_space:  global
        .offset:         24
        .size:           8
        .value_kind:     global_buffer
      - .actual_access:  read_only
        .address_space:  global
        .offset:         32
        .size:           8
        .value_kind:     global_buffer
      - .actual_access:  read_only
        .address_space:  global
        .offset:         40
        .size:           8
        .value_kind:     global_buffer
      - .actual_access:  read_only
        .address_space:  global
        .offset:         48
        .size:           8
        .value_kind:     global_buffer
      - .actual_access:  read_only
        .address_space:  global
        .offset:         56
        .size:           8
        .value_kind:     global_buffer
      - .actual_access:  read_only
        .address_space:  global
        .offset:         64
        .size:           8
        .value_kind:     global_buffer
      - .actual_access:  read_only
        .address_space:  global
        .offset:         72
        .size:           8
        .value_kind:     global_buffer
      - .actual_access:  write_only
        .address_space:  global
        .offset:         80
        .size:           8
        .value_kind:     global_buffer
    .group_segment_fixed_size: 70336
    .kernarg_segment_align: 8
    .kernarg_segment_size: 88
    .language:       OpenCL C
    .language_version:
      - 2
      - 0
    .max_flat_workgroup_size: 1024
    .name:           _Z13attend_kernelPKfS0_S0_S0_S0_S0_S0_S0_S0_S0_PDF16_
    .private_segment_fixed_size: 0
    .sgpr_count:     36
    .sgpr_spill_count: 0
    .symbol:         _Z13attend_kernelPKfS0_S0_S0_S0_S0_S0_S0_S0_S0_PDF16_.kd
    .uniform_work_group_size: 1
    .uses_dynamic_stack: false
    .vgpr_count:     86
    .vgpr_spill_count: 0
    .wavefront_size: 64
  - .agpr_count:     0
    .args:
      - .actual_access:  read_only
        .address_space:  global
        .offset:         0
        .size:           8
        .value_kind:     global_buffer
      - .actual_access:  read_only
        .address_space:  global
        .offset:         8
        .size:           8
        .value_kind:     global_buffer
      - .actual_access:  read_only
        .address_space:  global
        .offset:         16
        .size:           8
        .value_kind:     global_buffer
      - .actual_access:  read_only
        .address_space:  global
        .offset:         24
        .size:           8
        .value_kind:     global_buffer
      - .actual_access:  write_only
        .address_space:  global
        .offset:         32
        .size:           8
        .value_kind:     global_buffer
    .group_segment_fixed_size: 9088
    .kernarg_segment_align: 8
    .kernarg_segment_size: 40
    .language:       OpenCL C
    .language_version:
      - 2
      - 0
    .max_flat_workgroup_size: 512
    .name:           _Z16postfinal_kernelPKfS0_S0_S0_Pf
    .private_segment_fixed_size: 0
    .sgpr_count:     22
    .sgpr_spill_count: 0
    .symbol:         _Z16postfinal_kernelPKfS0_S0_S0_Pf.kd
    .uniform_work_group_size: 1
    .uses_dynamic_stack: false
    .vgpr_count:     124
    .vgpr_spill_count: 0
    .wavefront_size: 64
  - .agpr_count:     16
    .args:
      - .offset:         0
        .size:           1136
        .value_kind:     by_value
    .group_segment_fixed_size: 34816
    .kernarg_segment_align: 8
    .kernarg_segment_size: 1136
    .language:       OpenCL C
    .language_version:
      - 2
      - 0
    .max_flat_workgroup_size: 256
    .name:           _Z14gemm_nt_kernelILi2EEv8GemmArgs
    .private_segment_fixed_size: 0
    .sgpr_count:     68
    .sgpr_spill_count: 0
    .symbol:         _Z14gemm_nt_kernelILi2EEv8GemmArgs.kd
    .uniform_work_group_size: 1
    .uses_dynamic_stack: false
    .vgpr_count:     140
    .vgpr_spill_count: 0
    .wavefront_size: 64
  - .agpr_count:     0
    .args:
      - .actual_access:  read_only
        .address_space:  global
        .offset:         0
        .size:           8
        .value_kind:     global_buffer
      - .offset:         8
        .size:           8
        .value_kind:     by_value
      - .actual_access:  read_only
        .address_space:  global
        .offset:         16
        .size:           8
        .value_kind:     global_buffer
      - .actual_access:  read_only
        .address_space:  global
        .offset:         24
        .size:           8
        .value_kind:     global_buffer
      - .actual_access:  read_only
        .address_space:  global
        .offset:         32
        .size:           8
        .value_kind:     global_buffer
      - .actual_access:  read_only
        .address_space:  global
        .offset:         40
        .size:           8
        .value_kind:     global_buffer
      - .actual_access:  write_only
        .address_space:  global
        .offset:         48
        .size:           8
        .value_kind:     global_buffer
      - .actual_access:  write_only
        .address_space:  global
        .offset:         56
        .size:           8
        .value_kind:     global_buffer
      - .offset:         64
        .size:           4
        .value_kind:     by_value
      - .offset:         72
        .size:           376
        .value_kind:     by_value
    .group_segment_fixed_size: 62720
    .kernarg_segment_align: 8
    .kernarg_segment_size: 448
    .language:       OpenCL C
    .language_version:
      - 2
      - 0
    .max_flat_workgroup_size: 512
    .name:           _Z15gru_mfma_kernelILi1EEvPKfmS1_S1_S1_S1_PfS2_i7PreArgs
    .private_segment_fixed_size: 0
    .sgpr_count:     36
    .sgpr_spill_count: 0
    .symbol:         _Z15gru_mfma_kernelILi1EEvPKfmS1_S1_S1_S1_PfS2_i7PreArgs.kd
    .uniform_work_group_size: 1
    .uses_dynamic_stack: false
    .vgpr_count:     192
    .vgpr_spill_count: 0
    .wavefront_size: 64
  - .agpr_count:     0
    .args:
      - .actual_access:  read_only
        .address_space:  global
        .offset:         0
        .size:           8
        .value_kind:     global_buffer
      - .offset:         8
        .size:           8
        .value_kind:     by_value
      - .actual_access:  read_only
        .address_space:  global
        .offset:         16
        .size:           8
        .value_kind:     global_buffer
      - .actual_access:  read_only
        .address_space:  global
        .offset:         24
        .size:           8
        .value_kind:     global_buffer
      - .actual_access:  read_only
        .address_space:  global
        .offset:         32
        .size:           8
        .value_kind:     global_buffer
      - .actual_access:  read_only
        .address_space:  global
        .offset:         40
        .size:           8
        .value_kind:     global_buffer
      - .actual_access:  write_only
        .address_space:  global
        .offset:         48
        .size:           8
        .value_kind:     global_buffer
      - .actual_access:  write_only
        .address_space:  global
        .offset:         56
        .size:           8
        .value_kind:     global_buffer
      - .offset:         64
        .size:           4
        .value_kind:     by_value
      - .offset:         72
        .size:           376
        .value_kind:     by_value
    .group_segment_fixed_size: 64480
    .kernarg_segment_align: 8
    .kernarg_segment_size: 448
    .language:       OpenCL C
    .language_version:
      - 2
      - 0
    .max_flat_workgroup_size: 512
    .name:           _Z15gru_mfma_kernelILi2EEvPKfmS1_S1_S1_S1_PfS2_i7PreArgs
    .private_segment_fixed_size: 0
    .sgpr_count:     50
    .sgpr_spill_count: 0
    .symbol:         _Z15gru_mfma_kernelILi2EEvPKfmS1_S1_S1_S1_PfS2_i7PreArgs.kd
    .uniform_work_group_size: 1
    .uses_dynamic_stack: false
    .vgpr_count:     210
    .vgpr_spill_count: 0
    .wavefront_size: 64
